# speedup vs baseline: 1.0364x; 1.0364x over previous
.LBB0_2:
	s_or_b64 exec, exec, s[10:11]
	v_and_b32_e32 v34, 63, v0
	v_add_f32_dpp v35, v145, v145 row_ror:8 row_mask:0xf bank_mask:0xf bound_ctrl:1
	v_lshrrev_b32_e32 v39, 6, v0
	v_cmp_eq_u32_e64 s[6:7], 0, v34
	v_add_f32_dpp v35, v35, v35 row_ror:4 row_mask:0xf bank_mask:0xf bound_ctrl:1
	v_mov_b32_e32 v34, 0x3c0
	v_mad_u32_u24 v34, v39, 48, v34
	v_add_f32_dpp v35, v35, v35 row_ror:2 row_mask:0xf bank_mask:0xf bound_ctrl:1
	s_nop 1
	v_add_f32_dpp v35, v35, v35 row_ror:1 row_mask:0xf bank_mask:0xf bound_ctrl:1
	s_nop 0
	v_readlane_b32 s10, v35, 0
	v_readlane_b32 s12, v35, 16
	v_readlane_b32 s11, v35, 32
	v_readlane_b32 s13, v35, 48
	s_and_saveexec_b64 s[8:9], s[6:7]
	v_mov_b32_e32 v36, s12
	v_mov_b32_e32 v37, s13
	v_pk_add_f32 v[36:37], s[10:11], v[36:37]
	s_nop 0
	v_add_f32_e32 v35, v36, v37
	ds_write_b32 v34, v35
	s_or_b64 exec, exec, s[8:9]
	v_add_f32_dpp v35, v143, v143 row_ror:8 row_mask:0xf bank_mask:0xf bound_ctrl:1
	s_nop 1
	v_add_f32_dpp v35, v35, v35 row_ror:4 row_mask:0xf bank_mask:0xf bound_ctrl:1
	s_nop 1
	v_add_f32_dpp v35, v35, v35 row_ror:2 row_mask:0xf bank_mask:0xf bound_ctrl:1
	s_nop 1
	v_add_f32_dpp v35, v35, v35 row_ror:1 row_mask:0xf bank_mask:0xf bound_ctrl:1
	s_nop 0
	v_readlane_b32 s10, v35, 0
	v_readlane_b32 s12, v35, 16
	v_readlane_b32 s11, v35, 32
	v_readlane_b32 s13, v35, 48
	s_and_saveexec_b64 s[8:9], s[6:7]
	v_mov_b32_e32 v36, s12
	v_mov_b32_e32 v37, s13
	v_pk_add_f32 v[36:37], s[10:11], v[36:37]
	s_nop 0
	v_add_f32_e32 v35, v36, v37
	ds_write_b32 v34, v35 offset:4
	s_or_b64 exec, exec, s[8:9]
	v_add_f32_dpp v35, v144, v144 row_ror:8 row_mask:0xf bank_mask:0xf bound_ctrl:1
	s_nop 1
	v_add_f32_dpp v35, v35, v35 row_ror:4 row_mask:0xf bank_mask:0xf bound_ctrl:1
	s_nop 1
	v_add_f32_dpp v35, v35, v35 row_ror:2 row_mask:0xf bank_mask:0xf bound_ctrl:1
	s_nop 1
	v_add_f32_dpp v35, v35, v35 row_ror:1 row_mask:0xf bank_mask:0xf bound_ctrl:1
	s_nop 0
	v_readlane_b32 s10, v35, 0
	v_readlane_b32 s12, v35, 16
	v_readlane_b32 s11, v35, 32
	v_readlane_b32 s13, v35, 48
	s_and_saveexec_b64 s[8:9], s[6:7]
	v_mov_b32_e32 v36, s12
	v_mov_b32_e32 v37, s13
	v_pk_add_f32 v[36:37], s[10:11], v[36:37]
	s_nop 0
	v_add_f32_e32 v35, v36, v37
	ds_write_b32 v34, v35 offset:8
	s_or_b64 exec, exec, s[8:9]
	v_add_f32_dpp v35, v142, v142 row_ror:8 row_mask:0xf bank_mask:0xf bound_ctrl:1
	s_nop 1
	v_add_f32_dpp v35, v35, v35 row_ror:4 row_mask:0xf bank_mask:0xf bound_ctrl:1
	s_nop 1
	v_add_f32_dpp v35, v35, v35 row_ror:2 row_mask:0xf bank_mask:0xf bound_ctrl:1
	s_nop 1
	v_add_f32_dpp v35, v35, v35 row_ror:1 row_mask:0xf bank_mask:0xf bound_ctrl:1
	s_nop 0
	v_readlane_b32 s10, v35, 0
	v_readlane_b32 s12, v35, 16
	v_readlane_b32 s11, v35, 32
	v_readlane_b32 s13, v35, 48
	s_and_saveexec_b64 s[8:9], s[6:7]
	v_mov_b32_e32 v36, s12
	v_mov_b32_e32 v37, s13
	v_pk_add_f32 v[36:37], s[10:11], v[36:37]
	s_nop 0
	v_add_f32_e32 v35, v36, v37
	ds_write_b32 v34, v35 offset:12
	s_or_b64 exec, exec, s[8:9]
	v_add_f32_dpp v35, v141, v141 row_ror:8 row_mask:0xf bank_mask:0xf bound_ctrl:1
	s_nop 1
	v_add_f32_dpp v35, v35, v35 row_ror:4 row_mask:0xf bank_mask:0xf bound_ctrl:1
	s_nop 1
	v_add_f32_dpp v35, v35, v35 row_ror:2 row_mask:0xf bank_mask:0xf bound_ctrl:1
	s_nop 1
	v_add_f32_dpp v35, v35, v35 row_ror:1 row_mask:0xf bank_mask:0xf bound_ctrl:1
	s_nop 0
	v_readlane_b32 s10, v35, 0
	v_readlane_b32 s12, v35, 16
	v_readlane_b32 s11, v35, 32
	v_readlane_b32 s13, v35, 48
	s_and_saveexec_b64 s[8:9], s[6:7]
	v_mov_b32_e32 v36, s12
	v_mov_b32_e32 v37, s13
	v_pk_add_f32 v[36:37], s[10:11], v[36:37]
	s_nop 0
	v_add_f32_e32 v35, v36, v37
	ds_write_b32 v34, v35 offset:16
	s_or_b64 exec, exec, s[8:9]
	v_add_f32_dpp v35, v139, v139 row_ror:8 row_mask:0xf bank_mask:0xf bound_ctrl:1
	s_nop 1
	v_add_f32_dpp v35, v35, v35 row_ror:4 row_mask:0xf bank_mask:0xf bound_ctrl:1
	s_nop 1
	v_add_f32_dpp v35, v35, v35 row_ror:2 row_mask:0xf bank_mask:0xf bound_ctrl:1
	s_nop 1
	v_add_f32_dpp v35, v35, v35 row_ror:1 row_mask:0xf bank_mask:0xf bound_ctrl:1
	s_nop 0
	v_readlane_b32 s10, v35, 0
	v_readlane_b32 s12, v35, 16
	v_readlane_b32 s11, v35, 32
	v_readlane_b32 s13, v35, 48
	s_and_saveexec_b64 s[8:9], s[6:7]
	v_mov_b32_e32 v36, s12
	v_mov_b32_e32 v37, s13
	v_pk_add_f32 v[36:37], s[10:11], v[36:37]
	s_nop 0
	v_add_f32_e32 v35, v36, v37
	ds_write_b32 v34, v35 offset:20
	s_or_b64 exec, exec, s[8:9]
	v_add_f32_dpp v35, v140, v140 row_ror:8 row_mask:0xf bank_mask:0xf bound_ctrl:1
	s_nop 1
	v_add_f32_dpp v35, v35, v35 row_ror:4 row_mask:0xf bank_mask:0xf bound_ctrl:1
	s_nop 1
	v_add_f32_dpp v35, v35, v35 row_ror:2 row_mask:0xf bank_mask:0xf bound_ctrl:1
	s_nop 1
	v_add_f32_dpp v35, v35, v35 row_ror:1 row_mask:0xf bank_mask:0xf bound_ctrl:1
	s_nop 0
	v_readlane_b32 s10, v35, 0
	v_readlane_b32 s12, v35, 16
	v_readlane_b32 s11, v35, 32
	v_readlane_b32 s13, v35, 48
	s_and_saveexec_b64 s[8:9], s[6:7]
	v_mov_b32_e32 v36, s12
	v_mov_b32_e32 v37, s13
	v_pk_add_f32 v[36:37], s[10:11], v[36:37]
	s_nop 0
	v_add_f32_e32 v35, v36, v37
	ds_write_b32 v34, v35 offset:24
	s_or_b64 exec, exec, s[8:9]
	v_add_f32_dpp v35, v138, v138 row_ror:8 row_mask:0xf bank_mask:0xf bound_ctrl:1
	s_nop 1
	v_add_f32_dpp v35, v35, v35 row_ror:4 row_mask:0xf bank_mask:0xf bound_ctrl:1
	s_nop 1
	v_add_f32_dpp v35, v35, v35 row_ror:2 row_mask:0xf bank_mask:0xf bound_ctrl:1
	s_nop 1
	v_add_f32_dpp v35, v35, v35 row_ror:1 row_mask:0xf bank_mask:0xf bound_ctrl:1
	s_nop 0
	v_readlane_b32 s10, v35, 0
	v_readlane_b32 s12, v35, 16
	v_readlane_b32 s11, v35, 32
	v_readlane_b32 s13, v35, 48
	s_and_saveexec_b64 s[8:9], s[6:7]
	v_mov_b32_e32 v36, s12
	v_mov_b32_e32 v37, s13
	v_pk_add_f32 v[36:37], s[10:11], v[36:37]
	s_nop 0
	v_add_f32_e32 v35, v36, v37
	ds_write_b32 v34, v35 offset:28
	s_or_b64 exec, exec, s[8:9]
	v_add_f32_dpp v35, v137, v137 row_ror:8 row_mask:0xf bank_mask:0xf bound_ctrl:1
	s_nop 1
	v_add_f32_dpp v35, v35, v35 row_ror:4 row_mask:0xf bank_mask:0xf bound_ctrl:1
	s_nop 1
	v_add_f32_dpp v35, v35, v35 row_ror:2 row_mask:0xf bank_mask:0xf bound_ctrl:1
	s_nop 1
	v_add_f32_dpp v35, v35, v35 row_ror:1 row_mask:0xf bank_mask:0xf bound_ctrl:1
	s_nop 0
	v_readlane_b32 s10, v35, 0
	v_readlane_b32 s12, v35, 16
	v_readlane_b32 s11, v35, 32
	v_readlane_b32 s13, v35, 48
	s_and_saveexec_b64 s[8:9], s[6:7]
	v_mov_b32_e32 v36, s12
	v_mov_b32_e32 v37, s13
	v_pk_add_f32 v[36:37], s[10:11], v[36:37]
	s_nop 0
	v_add_f32_e32 v35, v36, v37
	ds_write_b32 v34, v35 offset:32
	s_or_b64 exec, exec, s[8:9]
	v_add_f32_dpp v35, v72, v72 row_ror:8 row_mask:0xf bank_mask:0xf bound_ctrl:1
	s_nop 1
	v_add_f32_dpp v35, v35, v35 row_ror:4 row_mask:0xf bank_mask:0xf bound_ctrl:1
	s_nop 1
	v_add_f32_dpp v35, v35, v35 row_ror:2 row_mask:0xf bank_mask:0xf bound_ctrl:1
	s_nop 1
	v_add_f32_dpp v35, v35, v35 row_ror:1 row_mask:0xf bank_mask:0xf bound_ctrl:1
	s_nop 0
	v_readlane_b32 s10, v35, 0
	v_readlane_b32 s12, v35, 16
	v_readlane_b32 s11, v35, 32
	v_readlane_b32 s13, v35, 48
	s_and_saveexec_b64 s[8:9], s[6:7]
	v_mov_b32_e32 v36, s12
	v_mov_b32_e32 v37, s13
	v_pk_add_f32 v[36:37], s[10:11], v[36:37]
	s_nop 0
	v_add_f32_e32 v35, v36, v37
	ds_write_b32 v34, v35 offset:36
	s_or_b64 exec, exec, s[8:9]
	v_add_f32_dpp v35, v73, v73 row_ror:8 row_mask:0xf bank_mask:0xf bound_ctrl:1
	s_nop 1
	v_add_f32_dpp v35, v35, v35 row_ror:4 row_mask:0xf bank_mask:0xf bound_ctrl:1
	s_nop 1
	v_add_f32_dpp v35, v35, v35 row_ror:2 row_mask:0xf bank_mask:0xf bound_ctrl:1
	s_nop 1
	v_add_f32_dpp v35, v35, v35 row_ror:1 row_mask:0xf bank_mask:0xf bound_ctrl:1
	s_nop 0
	v_readlane_b32 s10, v35, 0
	v_readlane_b32 s12, v35, 16
	v_readlane_b32 s11, v35, 32
	v_readlane_b32 s13, v35, 48
	s_and_saveexec_b64 s[8:9], s[6:7]
	v_mov_b32_e32 v36, s12
	v_mov_b32_e32 v37, s13
	v_pk_add_f32 v[36:37], s[10:11], v[36:37]
	s_nop 0
	v_add_f32_e32 v35, v36, v37
	ds_write_b32 v34, v35 offset:40
	s_or_b64 exec, exec, s[8:9]
	s_load_dwordx2 s[8:9], s[0:1], 0x10
	v_add_f32_dpp v35, v71, v71 row_ror:8 row_mask:0xf bank_mask:0xf bound_ctrl:1
	s_nop 1
	v_add_f32_dpp v35, v35, v35 row_ror:4 row_mask:0xf bank_mask:0xf bound_ctrl:1
	s_nop 1
	v_add_f32_dpp v35, v35, v35 row_ror:2 row_mask:0xf bank_mask:0xf bound_ctrl:1
	s_nop 1
	v_add_f32_dpp v35, v35, v35 row_ror:1 row_mask:0xf bank_mask:0xf bound_ctrl:1
	s_nop 0
	v_readlane_b32 s12, v35, 0
	v_readlane_b32 s14, v35, 16
	v_readlane_b32 s13, v35, 32
	v_readlane_b32 s15, v35, 48
	s_and_saveexec_b64 s[10:11], s[6:7]
	v_mov_b32_e32 v36, s14
	v_mov_b32_e32 v37, s15
	v_pk_add_f32 v[36:37], s[12:13], v[36:37]
	s_nop 0
	v_add_f32_e32 v35, v36, v37
	ds_write_b32 v34, v35 offset:44
	s_or_b64 exec, exec, s[10:11]
	v_cmp_gt_u32_e32 vcc, 12, v0
	v_lshlrev_b32_e32 v34, 2, v0
	s_waitcnt lgkmcnt(0)
	s_barrier
	s_load_dwordx4 s[12:15], s[0:1], 0x20
	s_load_dwordx2 s[10:11], s[0:1], 0x18
	s_mov_b32 s20, 0
	s_mov_b32 s21, 0xc1f00000
	s_mov_b32 s23, 0xffffffe0
	s_and_saveexec_b64 s[16:17], vcc
	s_cbranch_execz .Lkf_pub_done
	ds_read2_b32 v[36:37], v34 offset0:240 offset1:252
	v_add_u32_e32 v35, 0x400, v34
	ds_read2_b32 v[42:43], v35 offset0:8 offset1:20
	ds_read2_b32 v[44:45], v35 offset0:32 offset1:44
	ds_read2_b32 v[48:49], v35 offset0:56 offset1:68
	ds_read2_b32 v[52:53], v35 offset0:80 offset1:92
	ds_read2_b32 v[152:153], v35 offset0:104 offset1:116
	s_mul_i32 s18, s2, 48
	s_mul_hi_i32 s19, s2, 48
	s_waitcnt lgkmcnt(0)
	v_add_f32_e32 v36, 0, v36
	v_add_f32_e32 v36, v36, v37
	v_add_f32_e32 v36, v36, v42
	v_add_f32_e32 v36, v36, v43
	v_add_f32_e32 v36, v36, v44
	v_add_f32_e32 v36, v36, v45
	v_add_f32_e32 v36, v36, v48
	v_add_f32_e32 v36, v36, v49
	v_add_f32_e32 v36, v36, v52
	v_add_f32_e32 v36, v36, v53
	v_add_f32_e32 v36, v36, v152
	s_add_u32 s18, s8, s18
	v_add_f32_e32 v35, v36, v153
	s_addc_u32 s19, s9, s19
	v_and_b32_e32 v38, 3, v0
	v_lshrrev_b32_e32 v41, 2, v0
	global_store_dword v34, v35, s[18:19] sc1
	v_cmp_ne_u32_e32 vcc, 3, v38
	s_and_b64 exec, exec, vcc
	s_cbranch_execz .Lkf_pub_done
	v_cmp_eq_u32_e32 vcc, 0, v38
	v_cvt_f64_f32_e32 v[42:43], v35
	s_lshl_b32 s18, s24, 4
	s_add_i32 s18, s18, s3
	v_cndmask_b32_e64 v37, 24, 0, vcc
	v_ldexp_f64 v[42:43], v[42:43], v37
	s_mulk_i32 s18, 0x60
	v_lshlrev_b32_e32 v41, 5, v41
	v_ldexp_f64 v[44:45], v[42:43], s23
	v_lshl_add_u32 v41, v38, 3, v41
	v_floor_f64_e32 v[44:45], v[44:45]
	v_add_u32_e32 v41, s18, v41
	v_fma_f64 v[48:49], v[44:45], s[20:21], v[42:43]
	v_cvt_i32_f64_e32 v37, v[44:45]
	v_cvt_u32_f64_e32 v36, v[48:49]
	s_nop 0
	v_lshlrev_b64 v[36:37], 8, v[36:37]
	s_nop 0
	v_or_b32_e32 v36, 1, v36
	s_nop 0
	global_atomic_add_x2 v41, v[36:37], s[14:15]
.Lkf_pub_done:
	s_or_b64 exec, exec, s[16:17]
	v_cmp_lt_u32_e32 vcc, 63, v0
	s_and_saveexec_b64 s[16:17], vcc
	s_cbranch_execz .Lkf_zero_done
	v_mov_b32_e32 v36, 0x670
	v_lshl_add_u32 v36, v0, 2, v36
	v_add_u32_e32 v35, 0xfffffd00, v0
	v_add_u32_e32 v36, 0xffffff00, v36
	s_mov_b64 s[18:19], 0
	v_mov_b32_e32 v37, 0
	s_movk_i32 s22, 0x2d3f
.Lkf_zero_loop:
	v_add_u32_e32 v35, 0x2c0, v35
	v_cmp_lt_i32_e32 vcc, s22, v35
	ds_write_b32 v36, v37
	s_or_b64 s[18:19], vcc, s[18:19]
	v_add_u32_e32 v36, 0xb00, v36
	s_andn2_b64 exec, exec, s[18:19]
	s_cbranch_execnz .Lkf_zero_loop
.Lkf_zero_done:
	s_or_b64 exec, exec, s[16:17]
	v_cmp_ne_u32_e64 s[0:1], 0, v0
	v_cmp_gt_u32_e32 vcc, 48, v0
	s_and_saveexec_b64 s[16:17], vcc
	s_cbranch_execz .Lkf_par_done
	v_lshrrev_b32_e32 v35, 4, v0
	v_and_b32_e32 v36, 15, v0
	v_lshl_add_u32 v37, s24, 4, v36
	v_mad_u32_u24 v37, v37, 3, v35
	v_lshlrev_b32_e32 v38, 5, v37
	v_cmp_eq_u32_e64 s[18:19], s3, v36
	v_lshlrev_b32_e32 v154, 2, v35
	s_mov_b32 s22, 0x40000
.Lkf_poll:
	global_load_dwordx4 v[42:45], v38, s[14:15] sc1
	global_load_dwordx2 v[48:49], v38, s[14:15] offset:16 sc1
	s_add_i32 s22, s22, -1
	s_waitcnt vmcnt(0)
	v_and_b32_e32 v36, 0xff, v42
	v_and_b32_e32 v37, 0xff, v44
	v_and_b32_e32 v41, 0xff, v48
	v_add3_u32 v36, v36, v37, v41
	v_cmp_ne_u32_e32 vcc, 24, v36
	s_cmp_eq_u32 s22, 0
	s_cbranch_scc1 .Lkf_poll_end
	s_cbranch_vccz .Lkf_poll_end
	s_sleep 1
	s_branch .Lkf_poll
.Lkf_poll_end:
	v_lshrrev_b32_e32 v36, 8, v42
	v_and_b32_e32 v44, 0xffffff00, v44
	v_and_b32_e32 v48, 0xffffff00, v48
	v_cvt_f32_u32_e32 v36, v36
	v_cvt_f64_i32_e32 v[52:53], v45
	v_cvt_f64_u32_e32 v[152:153], v44
	v_cvt_f64_i32_e32 v[42:43], v49
	v_cvt_f64_u32_e32 v[44:45], v48
	v_ldexp_f64 v[52:53], v[52:53], 32
	v_ldexp_f64 v[42:43], v[42:43], 32
	v_add_f64 v[52:53], v[52:53], v[152:153]
	v_add_f64 v[42:43], v[42:43], v[44:45]
	v_ldexp_f64 v[52:53], v[52:53], s23
	v_ldexp_f64 v[42:43], v[42:43], s23
	v_cvt_f32_f64_e32 v37, v[52:53]
	v_cvt_f32_f64_e32 v49, v[42:43]
	s_nop 0
	v_div_scale_f32 v35, s[20:21], v36, v36, v37
	v_rcp_f32_e32 v38, v35
	v_div_scale_f32 v41, vcc, v37, v36, v37
	v_fma_f32 v42, -v35, v38, 1.0
	v_fmac_f32_e32 v38, v42, v38
	v_mul_f32_e32 v42, v41, v38
	v_fma_f32 v43, -v35, v42, v41
	v_fmac_f32_e32 v42, v43, v38
	v_fma_f32 v35, -v35, v42, v41
	v_div_fmas_f32 v35, v35, v38, v42
	v_div_fixup_f32 v35, v35, v36, v37
	v_div_scale_f32 v38, s[20:21], v36, v36, v49
	v_rcp_f32_e32 v41, v38
	v_div_scale_f32 v44, vcc, v49, v36, v49
	v_fma_f32 v42, -v38, v41, 1.0
	v_fmac_f32_e32 v41, v42, v41
	v_mul_f32_e32 v45, v44, v41
	v_fma_f32 v48, -v38, v45, v44
	v_fmac_f32_e32 v45, v48, v41
	v_fma_f32 v38, -v38, v45, v44
	v_div_fmas_f32 v38, v38, v41, v45
	v_div_fixup_f32 v38, v38, v36, v49
	v_add_f32_dpp v35, v35, v35 row_ror:8 row_mask:0xf bank_mask:0xf bound_ctrl:1
	v_mul_f32_e32 v38, 0x41200000, v38
	s_mov_b32 s20, 0x3fb8aa3b
	v_add_f32_dpp v35, v35, v35 row_ror:4 row_mask:0xf bank_mask:0xf bound_ctrl:1
	v_mul_f32_e32 v41, 0x3fb8aa3b, v38
	v_rndne_f32_e32 v43, v41
	v_add_f32_dpp v35, v35, v35 row_ror:2 row_mask:0xf bank_mask:0xf bound_ctrl:1
	v_fma_f32 v42, v38, s20, -v41
	v_fmamk_f32 v42, v38, 0x32a5705f, v42
	v_add_f32_dpp v35, v35, v35 row_ror:1 row_mask:0xf bank_mask:0xf bound_ctrl:1
	v_sub_f32_e32 v41, v41, v43
	v_add_f32_e32 v41, v41, v42
	v_exp_f32_e32 v41, v41
	v_cvt_i32_f32_e32 v42, v43
	s_mov_b32 s20, 0xc2ce8ed0
	s_mov_b32 s21, 0x42b17218
	v_cmp_ngt_f32_e32 vcc, s20, v38
	v_ldexp_f32 v36, v41, v42
	v_mul_f32_e32 v35, 0x3caaaaab, v35
	v_cndmask_b32_e32 v36, 0, v36, vcc
	v_mov_b32_e32 v37, 0x7f800000
	v_cmp_nlt_f32_e32 vcc, s21, v38
	s_nop 1
	v_cndmask_b32_e32 v36, v37, v36, vcc
	v_mul_f32_e32 v36, 0xbfb8aa3b, v36
	v_add_f32_e32 v37, v35, v35
	v_mul_f32_e64 v37, v37, -v36
	v_mul_f32_e32 v38, 0x40400000, v35
	v_mul_f32_e32 v35, v35, v38
	v_mul_f32_e32 v35, v35, v36
	s_and_b64 exec, exec, s[18:19]
	ds_write_b32 v154, v36 offset:1600
	ds_write_b32 v154, v37 offset:1612
	ds_write_b32 v154, v35 offset:1624
.Lkf_par_done:
	s_mov_b64 exec, -1
	v_lshlrev_b32_e32 v4, 4, v4
	v_lshlrev_b32_e32 v5, 6, v5
	v_lshl_or_b32 v3, v3, 2, v4
	v_lshlrev_b32_e32 v4, 4, v12
	v_or3_b32 v3, v3, v5, v2
	v_lshlrev_b32_e32 v5, 6, v13
	v_lshl_or_b32 v4, v11, 2, v4
	v_or3_b32 v43, v4, v5, v10
	v_lshlrev_b32_e32 v4, 4, v16
	v_lshlrev_b32_e32 v5, 6, v17
	v_lshl_or_b32 v4, v15, 2, v4
	v_lshlrev_b32_e32 v8, 4, v8
	v_or3_b32 v42, v4, v5, v14
	v_lshlrev_b32_e32 v4, 4, v20
	v_lshlrev_b32_e32 v9, 6, v9
	v_lshl_or_b32 v7, v7, 2, v8
	v_lshlrev_b32_e32 v5, 6, v21
	v_lshl_or_b32 v4, v19, 2, v4
	v_or3_b32 v44, v7, v9, v6
	v_or3_b32 v41, v4, v5, v18
	v_lshlrev_b32_e32 v4, 4, v24
	v_mov_b32_e32 v7, 0
	v_mov_b32_e32 v8, 0x64c
	v_lshlrev_b32_e32 v5, 6, v25
	v_lshl_or_b32 v4, v23, 2, v4
	s_waitcnt lgkmcnt(0)
	s_barrier
	ds_read_b96 v[36:38], v7 offset:1600
	ds_read_b64 v[16:17], v7 offset:1624
	ds_read2_b32 v[20:21], v8 offset1:1
	v_or3_b32 v19, v4, v5, v22
	v_lshlrev_b32_e32 v4, 4, v28
	v_lshlrev_b32_e32 v5, 6, v29
	v_lshl_or_b32 v4, v27, 2, v4
	v_or3_b32 v13, v4, v5, v26
	v_lshlrev_b32_e32 v4, 4, v32
	v_lshlrev_b32_e32 v5, 6, v33
	v_lshl_or_b32 v4, v31, 2, v4
	v_or3_b32 v9, v4, v5, v30
	s_waitcnt lgkmcnt(0)
	v_pk_fma_f32 v[4:5], v[76:77], v[20:21], v[16:17] op_sel_hi:[1,0,0]
	ds_read_b32 v8, v7 offset:1620
	ds_read_b32 v12, v7 offset:1632
	v_pk_fma_f32 v[4:5], v[78:79], v[36:37], v[4:5] op_sel_hi:[1,0,1]
	v_and_b32_e32 v6, 3, v6
	v_exp_f32_e32 v4, v4
	v_exp_f32_e32 v7, v5
	s_movk_i32 s3, 0xfff
	v_cmp_eq_u32_e32 vcc, 1, v6
	ds_read_b128 v[32:35], v134 offset:49152
	v_cvt_pknorm_u16_f32 v5, v4, v7
	v_lshrrev_b32_e32 v11, 4, v5
	v_bfe_u32 v15, v5, 4, 12
	v_bitop3_b32 v11, v11, s3, v11 bitop3:0xc
	v_cndmask_b32_e32 v15, v15, v11, vcc
	v_mov_b32_e32 v11, 0x670
	v_lshl_add_u32 v25, v15, 2, v11
	v_mov_b32_e32 v15, 0x10000
	v_cndmask_b32_e32 v27, 1, v15, vcc
	v_bfe_u32 v23, v44, 2, 2
	ds_add_u32 v25, v27
	v_cndmask_b32_e32 v25, 0, v4, vcc
	v_lshrrev_b32_e32 v4, 20, v5
	v_xor_b32_e32 v5, 0xfff, v4
	v_cmp_eq_u32_e32 vcc, 1, v23
	v_mov_b32_e32 v24, v38
	s_nop 0
	v_cndmask_b32_e32 v4, v4, v5, vcc
	v_lshl_add_u32 v27, v4, 2, v11
	v_pk_fma_f32 v[4:5], v[76:77], v[20:21], v[16:17] op_sel:[0,1,1]
	v_cndmask_b32_e32 v7, 0, v7, vcc
	v_pk_fma_f32 v[4:5], v[78:79], v[36:37], v[4:5] op_sel:[0,1,0]
	s_nop 0
	v_exp_f32_e32 v4, v4
	v_exp_f32_e32 v28, v5
	v_cndmask_b32_e32 v5, 1, v15, vcc
	ds_add_u32 v27, v5
	v_cmp_eq_u32_e32 vcc, 2, v6
	v_cvt_pknorm_u16_f32 v5, v4, v28
	v_lshrrev_b32_e32 v27, 4, v5
	v_bfe_u32 v29, v5, 4, 12
	v_bitop3_b32 v27, v27, s3, v27 bitop3:0xc
	v_cndmask_b32_e32 v25, v25, v4, vcc
	v_lshrrev_b32_e32 v4, 20, v5
	v_cndmask_b32_e32 v27, v29, v27, vcc
	v_cndmask_b32_e32 v29, 1, v15, vcc
	v_xor_b32_e32 v5, 0xfff, v4
	v_cmp_eq_u32_e32 vcc, 2, v23
	v_lshl_add_u32 v27, v27, 2, v11
	ds_add_u32 v27, v29 offset:16384
	v_cndmask_b32_e32 v4, v4, v5, vcc
	v_lshl_add_u32 v27, v4, 2, v11
	s_waitcnt lgkmcnt(4)
	v_pk_fma_f32 v[4:5], v[76:77], v[8:9], v[12:13] op_sel_hi:[1,0,0]
	v_cndmask_b32_e32 v29, 1, v15, vcc
	v_pk_fma_f32 v[4:5], v[78:79], v[24:25], v[4:5] op_sel_hi:[1,0,1]
	ds_add_u32 v27, v29 offset:16384
	v_exp_f32_e32 v4, v4
	v_exp_f32_e32 v5, v5
	v_cndmask_b32_e32 v7, v7, v28, vcc
	v_cmp_eq_u32_e32 vcc, 3, v6
	v_cvt_pknorm_u16_f32 v27, v4, v5
	v_lshrrev_b32_e32 v28, 4, v27
	v_bfe_u32 v29, v27, 4, 12
	v_bitop3_b32 v28, v28, s3, v28 bitop3:0xc
	v_cndmask_b32_e32 v6, v29, v28, vcc
	v_lshl_add_u32 v6, v6, 2, v11
	v_cndmask_b32_e32 v28, 1, v15, vcc
	ds_add_u32 v6, v28 offset:32768
	v_lshrrev_b32_e32 v6, 20, v27
	v_cndmask_b32_e32 v4, v25, v4, vcc
	v_xor_b32_e32 v25, 0xfff, v6
	v_cmp_eq_u32_e32 vcc, 3, v23
	v_bfe_u32 v27, v44, 6, 2
	s_nop 0
	v_cndmask_b32_e32 v6, v6, v25, vcc
	v_lshl_add_u32 v6, v6, 2, v11
	v_cndmask_b32_e32 v23, 1, v15, vcc
	ds_add_u32 v6, v23 offset:32768
	v_cndmask_b32_e32 v5, v7, v5, vcc
	v_pk_fma_f32 v[6:7], v[20:21], v[80:81], v[16:17] op_sel_hi:[0,1,0]
	v_pk_fma_f32 v[6:7], v[36:37], v[82:83], v[6:7] op_sel_hi:[0,1,1]
	v_exp_f32_e32 v6, v6
	v_exp_f32_e32 v23, v7
	v_bfe_u32 v25, v44, 4, 2
	v_cmp_eq_u32_e32 vcc, 1, v25
	s_waitcnt lgkmcnt(6)
	v_pk_add_f32 v[4:5], v[32:33], v[4:5] neg_lo:[0,1] neg_hi:[0,1]
	v_cvt_pknorm_u16_f32 v7, v6, v23
	v_lshrrev_b32_e32 v28, 4, v7
	v_bfe_u32 v29, v7, 4, 12
	v_bitop3_b32 v28, v28, s3, v28 bitop3:0xc
	v_cndmask_b32_e32 v28, v29, v28, vcc
	v_lshl_add_u32 v28, v28, 2, v11
	v_cndmask_b32_e32 v29, 1, v15, vcc
	ds_add_u32 v28, v29
	v_cndmask_b32_e32 v28, 0, v6, vcc
	v_lshrrev_b32_e32 v6, 20, v7
	v_xor_b32_e32 v7, 0xfff, v6
	v_cmp_eq_u32_e32 vcc, 1, v27
	s_nop 1
	v_cndmask_b32_e32 v6, v6, v7, vcc
	v_lshl_add_u32 v29, v6, 2, v11
	v_pk_fma_f32 v[6:7], v[20:21], v[80:81], v[16:17] op_sel:[1,0,1]
	v_cndmask_b32_e32 v23, 0, v23, vcc
	v_pk_fma_f32 v[6:7], v[36:37], v[82:83], v[6:7] op_sel:[1,0,0]
	s_nop 0
	v_exp_f32_e32 v6, v6
	v_exp_f32_e32 v31, v7
	v_cndmask_b32_e32 v7, 1, v15, vcc
	ds_add_u32 v29, v7
	v_cmp_eq_u32_e32 vcc, 2, v25
	v_cvt_pknorm_u16_f32 v7, v6, v31
	v_lshrrev_b32_e32 v29, 4, v7
	v_bfe_u32 v32, v7, 4, 12
	v_bitop3_b32 v29, v29, s3, v29 bitop3:0xc
	v_cndmask_b32_e32 v28, v28, v6, vcc
	v_lshrrev_b32_e32 v6, 20, v7
	v_cndmask_b32_e32 v29, v32, v29, vcc
	v_cndmask_b32_e32 v32, 1, v15, vcc
	v_xor_b32_e32 v7, 0xfff, v6
	v_cmp_eq_u32_e32 vcc, 2, v27
	v_lshl_add_u32 v29, v29, 2, v11
	ds_add_u32 v29, v32 offset:16384
	v_cndmask_b32_e32 v6, v6, v7, vcc
	v_lshl_add_u32 v29, v6, 2, v11
	v_pk_fma_f32 v[6:7], v[8:9], v[80:81], v[12:13] op_sel_hi:[0,1,0]
	v_pk_fma_f32 v[6:7], v[24:25], v[82:83], v[6:7] op_sel_hi:[0,1,1]
	v_exp_f32_e32 v6, v6
	v_exp_f32_e32 v7, v7
	v_cndmask_b32_e32 v32, 1, v15, vcc
	ds_add_u32 v29, v32 offset:16384
	v_cndmask_b32_e32 v23, v23, v31, vcc
	v_cvt_pknorm_u16_f32 v29, v6, v7
	v_lshrrev_b32_e32 v31, 4, v29
	v_bfe_u32 v32, v29, 4, 12
	v_bitop3_b32 v31, v31, s3, v31 bitop3:0xc
	v_cmp_eq_u32_e32 vcc, 3, v25
	s_nop 1
	v_cndmask_b32_e32 v25, v32, v31, vcc
	v_lshl_add_u32 v25, v25, 2, v11
	v_cndmask_b32_e32 v31, 1, v15, vcc
	ds_add_u32 v25, v31 offset:32768
	v_lshrrev_b32_e32 v25, 20, v29
	v_cndmask_b32_e32 v6, v28, v6, vcc
	v_xor_b32_e32 v28, 0xfff, v25
	v_cmp_eq_u32_e32 vcc, 3, v27
	s_nop 1
	v_cndmask_b32_e32 v25, v25, v28, vcc
	v_lshl_add_u32 v25, v25, 2, v11
	v_cndmask_b32_e32 v27, 1, v15, vcc
	ds_add_u32 v25, v27 offset:32768
	v_cndmask_b32_e32 v7, v23, v7, vcc
	v_pk_add_f32 v[6:7], v[34:35], v[6:7] neg_lo:[0,1] neg_hi:[0,1]
	s_nop 0
	v_pk_mul_f32 v[6:7], v[6:7], v[6:7]
	s_nop 0
	v_pk_fma_f32 v[28:29], v[4:5], v[4:5], v[6:7]
	v_pk_fma_f32 v[4:5], v[84:85], v[20:21], v[16:17] op_sel_hi:[1,0,0]
	v_and_b32_e32 v2, 3, v2
	v_pk_fma_f32 v[4:5], v[86:87], v[36:37], v[4:5] op_sel_hi:[1,0,1]
	v_cmp_eq_u32_e32 vcc, 1, v2
	v_exp_f32_e32 v23, v4
	v_exp_f32_e32 v25, v5
	v_bfe_u32 v27, v3, 2, 2
	ds_read_b128 v[4:7], v134 offset:61440
	v_cvt_pknorm_u16_f32 v31, v23, v25
	v_lshrrev_b32_e32 v32, 4, v31
	v_bfe_u32 v33, v31, 4, 12
	v_bitop3_b32 v32, v32, s3, v32 bitop3:0xc
	v_cndmask_b32_e32 v32, v33, v32, vcc
	v_lshl_add_u32 v32, v32, 2, v11
	v_cndmask_b32_e32 v33, 1, v15, vcc
	v_lshrrev_b32_e32 v31, 20, v31
	ds_add_u32 v32, v33
	v_cndmask_b32_e32 v23, 0, v23, vcc
	v_xor_b32_e32 v32, 0xfff, v31
	v_cmp_eq_u32_e32 vcc, 1, v27
	s_nop 1
	v_cndmask_b32_e32 v31, v31, v32, vcc
	v_pk_fma_f32 v[32:33], v[84:85], v[20:21], v[16:17] op_sel:[0,1,1]
	v_lshl_add_u32 v31, v31, 2, v11
	v_pk_fma_f32 v[32:33], v[86:87], v[36:37], v[32:33] op_sel:[0,1,0]
	v_cndmask_b32_e32 v25, 0, v25, vcc
	v_exp_f32_e32 v32, v32
	v_exp_f32_e32 v34, v33
	v_cndmask_b32_e32 v33, 1, v15, vcc
	ds_add_u32 v31, v33
	v_cmp_eq_u32_e32 vcc, 2, v2
	v_cvt_pknorm_u16_f32 v31, v32, v34
	v_lshrrev_b32_e32 v33, 4, v31
	v_bfe_u32 v35, v31, 4, 12
	v_bitop3_b32 v33, v33, s3, v33 bitop3:0xc
	v_cndmask_b32_e32 v33, v35, v33, vcc
	v_lshrrev_b32_e32 v31, 20, v31
	v_lshl_add_u32 v33, v33, 2, v11
	v_cndmask_b32_e32 v35, 1, v15, vcc
	v_cndmask_b32_e32 v23, v23, v32, vcc
	v_xor_b32_e32 v32, 0xfff, v31
	v_cmp_eq_u32_e32 vcc, 2, v27
	ds_add_u32 v33, v35 offset:16384
	s_nop 0
	v_cndmask_b32_e32 v31, v31, v32, vcc
	v_pk_fma_f32 v[32:33], v[84:85], v[8:9], v[12:13] op_sel_hi:[1,0,0]
	v_lshl_add_u32 v31, v31, 2, v11
	v_pk_fma_f32 v[32:33], v[86:87], v[24:25], v[32:33] op_sel_hi:[1,0,1]
	v_cndmask_b32_e32 v35, 1, v15, vcc
	v_exp_f32_e32 v32, v32
	v_exp_f32_e32 v33, v33
	ds_add_u32 v31, v35 offset:16384
	v_cndmask_b32_e32 v25, v25, v34, vcc
	v_cmp_eq_u32_e32 vcc, 3, v2
	v_cvt_pknorm_u16_f32 v31, v32, v33
	v_lshrrev_b32_e32 v34, 4, v31
	v_bfe_u32 v35, v31, 4, 12
	v_bitop3_b32 v34, v34, s3, v34 bitop3:0xc
	v_cndmask_b32_e32 v2, v35, v34, vcc
	v_lshl_add_u32 v2, v2, 2, v11
	v_cndmask_b32_e32 v34, 1, v15, vcc
	ds_add_u32 v2, v34 offset:32768
	v_cndmask_b32_e32 v32, v23, v32, vcc
	v_lshrrev_b32_e32 v2, 20, v31
	v_cmp_eq_u32_e32 vcc, 3, v27
	v_xor_b32_e32 v23, 0xfff, v2
	v_bfe_u32 v27, v3, 6, 2
	v_cndmask_b32_e32 v33, v25, v33, vcc
	v_cndmask_b32_e32 v2, v2, v23, vcc
	s_waitcnt lgkmcnt(5)
	v_pk_add_f32 v[4:5], v[4:5], v[32:33] neg_lo:[0,1] neg_hi:[0,1]
	v_pk_fma_f32 v[32:33], v[20:21], v[88:89], v[16:17] op_sel_hi:[0,1,0]
	v_lshl_add_u32 v2, v2, 2, v11
	v_cndmask_b32_e32 v23, 1, v15, vcc
	v_pk_fma_f32 v[32:33], v[36:37], v[90:91], v[32:33] op_sel_hi:[0,1,1]
	ds_add_u32 v2, v23 offset:32768
	v_exp_f32_e32 v2, v32
	v_exp_f32_e32 v23, v33
	v_bfe_u32 v25, v3, 4, 2
	v_pk_fma_f32 v[4:5], v[4:5], v[4:5], v[28:29]
	v_cmp_eq_u32_e32 vcc, 1, v25
	v_cvt_pknorm_u16_f32 v3, v2, v23
	v_lshrrev_b32_e32 v28, 4, v3
	v_bfe_u32 v29, v3, 4, 12
	v_bitop3_b32 v28, v28, s3, v28 bitop3:0xc
	v_cndmask_b32_e32 v28, v29, v28, vcc
	v_lshl_add_u32 v28, v28, 2, v11
	v_cndmask_b32_e32 v29, 1, v15, vcc
	ds_add_u32 v28, v29
	v_cndmask_b32_e32 v28, 0, v2, vcc
	v_lshrrev_b32_e32 v2, 20, v3
	v_xor_b32_e32 v3, 0xfff, v2
	v_cmp_eq_u32_e32 vcc, 1, v27
	v_cmp_eq_u32_e64 s[8:9], 3, v27
	s_nop 0
	v_cndmask_b32_e32 v2, v2, v3, vcc
	v_lshl_add_u32 v29, v2, 2, v11
	v_pk_fma_f32 v[2:3], v[20:21], v[88:89], v[16:17] op_sel:[1,0,1]
	v_cndmask_b32_e32 v23, 0, v23, vcc
	v_pk_fma_f32 v[2:3], v[36:37], v[90:91], v[2:3] op_sel:[1,0,0]
	s_nop 0
	v_exp_f32_e32 v2, v2
	v_exp_f32_e32 v31, v3
	v_cndmask_b32_e32 v3, 1, v15, vcc
	ds_add_u32 v29, v3
	v_cmp_eq_u32_e32 vcc, 2, v25
	v_cvt_pknorm_u16_f32 v3, v2, v31
	v_lshrrev_b32_e32 v29, 4, v3
	v_bfe_u32 v32, v3, 4, 12
	v_bitop3_b32 v29, v29, s3, v29 bitop3:0xc
	v_cndmask_b32_e32 v28, v28, v2, vcc
	v_lshrrev_b32_e32 v2, 20, v3
	v_cndmask_b32_e32 v29, v32, v29, vcc
	v_cndmask_b32_e32 v32, 1, v15, vcc
	v_xor_b32_e32 v3, 0xfff, v2
	v_cmp_eq_u32_e32 vcc, 2, v27
	v_lshl_add_u32 v29, v29, 2, v11
	ds_add_u32 v29, v32 offset:16384
	v_cndmask_b32_e32 v2, v2, v3, vcc
	v_lshl_add_u32 v29, v2, 2, v11
	v_pk_fma_f32 v[2:3], v[8:9], v[88:89], v[12:13] op_sel_hi:[0,1,0]
	v_pk_fma_f32 v[2:3], v[24:25], v[90:91], v[2:3] op_sel_hi:[0,1,1]
	v_exp_f32_e32 v2, v2
	v_exp_f32_e32 v3, v3
	v_cndmask_b32_e32 v32, 1, v15, vcc
	ds_add_u32 v29, v32 offset:16384
	v_cndmask_b32_e32 v23, v23, v31, vcc
	v_cvt_pknorm_u16_f32 v29, v2, v3
	v_lshrrev_b32_e32 v31, 4, v29
	v_bfe_u32 v32, v29, 4, 12
	v_bitop3_b32 v31, v31, s3, v31 bitop3:0xc
	v_cmp_eq_u32_e32 vcc, 3, v25
	v_cndmask_b32_e64 v27, 1, v15, s[8:9]
	v_cndmask_b32_e64 v3, v23, v3, s[8:9]
	v_cndmask_b32_e32 v25, v32, v31, vcc
	v_lshl_add_u32 v25, v25, 2, v11
	v_cndmask_b32_e32 v31, 1, v15, vcc
	ds_add_u32 v25, v31 offset:32768
	v_lshrrev_b32_e32 v25, 20, v29
	v_xor_b32_e32 v29, 0xfff, v25
	v_cndmask_b32_e64 v25, v25, v29, s[8:9]
	v_lshl_add_u32 v25, v25, 2, v11
	ds_add_u32 v25, v27 offset:32768
	v_cndmask_b32_e32 v2, v28, v2, vcc
	v_pk_add_f32 v[2:3], v[6:7], v[2:3] neg_lo:[0,1] neg_hi:[0,1]
	s_nop 0
	v_pk_fma_f32 v[6:7], v[2:3], v[2:3], v[4:5]
	v_pk_fma_f32 v[2:3], v[92:93], v[20:21], v[16:17] op_sel_hi:[1,0,0]
	v_and_b32_e32 v10, 3, v10
	v_pk_fma_f32 v[2:3], v[94:95], v[36:37], v[2:3] op_sel_hi:[1,0,1]
	v_cmp_eq_u32_e32 vcc, 1, v10
	v_exp_f32_e32 v23, v2
	v_exp_f32_e32 v25, v3
	v_bfe_u32 v27, v43, 2, 2
	ds_read_b128 v[2:5], v1 offset:24576
	v_cvt_pknorm_u16_f32 v28, v23, v25
	v_lshrrev_b32_e32 v29, 4, v28
	v_bfe_u32 v31, v28, 4, 12
	v_bitop3_b32 v29, v29, s3, v29 bitop3:0xc
	v_cndmask_b32_e32 v29, v31, v29, vcc
	v_lshl_add_u32 v29, v29, 2, v11
	v_cndmask_b32_e32 v31, 1, v15, vcc
	v_lshrrev_b32_e32 v28, 20, v28
	ds_add_u32 v29, v31
	v_cndmask_b32_e32 v23, 0, v23, vcc
	v_xor_b32_e32 v29, 0xfff, v28
	v_cmp_eq_u32_e32 vcc, 1, v27
	s_nop 1
	v_cndmask_b32_e32 v28, v28, v29, vcc
	v_lshl_add_u32 v31, v28, 2, v11
	v_pk_fma_f32 v[28:29], v[92:93], v[20:21], v[16:17] op_sel:[0,1,1]
	v_cndmask_b32_e32 v25, 0, v25, vcc
	v_pk_fma_f32 v[28:29], v[94:95], v[36:37], v[28:29] op_sel:[0,1,0]
	s_nop 0
	v_exp_f32_e32 v28, v28
	v_exp_f32_e32 v32, v29
	v_cndmask_b32_e32 v29, 1, v15, vcc
	ds_add_u32 v31, v29
	v_cmp_eq_u32_e32 vcc, 2, v10
	v_cvt_pknorm_u16_f32 v29, v28, v32
	v_lshrrev_b32_e32 v31, 4, v29
	v_bfe_u32 v33, v29, 4, 12
	v_bitop3_b32 v31, v31, s3, v31 bitop3:0xc
	v_cndmask_b32_e32 v23, v23, v28, vcc
	v_lshrrev_b32_e32 v28, 20, v29
	v_cndmask_b32_e32 v31, v33, v31, vcc
	v_cndmask_b32_e32 v33, 1, v15, vcc
	v_xor_b32_e32 v29, 0xfff, v28
	v_cmp_eq_u32_e32 vcc, 2, v27
	v_lshl_add_u32 v31, v31, 2, v11
	ds_add_u32 v31, v33 offset:16384
	v_cndmask_b32_e32 v28, v28, v29, vcc
	v_lshl_add_u32 v31, v28, 2, v11
	v_pk_fma_f32 v[28:29], v[92:93], v[8:9], v[12:13] op_sel_hi:[1,0,0]
	v_cndmask_b32_e32 v33, 1, v15, vcc
	v_pk_fma_f32 v[28:29], v[94:95], v[24:25], v[28:29] op_sel_hi:[1,0,1]
	ds_add_u32 v31, v33 offset:16384
	v_exp_f32_e32 v28, v28
	v_exp_f32_e32 v29, v29
	v_cndmask_b32_e32 v25, v25, v32, vcc
	v_cmp_eq_u32_e32 vcc, 3, v10
	v_cvt_pknorm_u16_f32 v31, v28, v29
	v_lshrrev_b32_e32 v32, 4, v31
	v_bfe_u32 v33, v31, 4, 12
	v_bitop3_b32 v32, v32, s3, v32 bitop3:0xc
	v_cndmask_b32_e32 v10, v33, v32, vcc
	v_lshl_add_u32 v10, v10, 2, v11
	v_cndmask_b32_e32 v32, 1, v15, vcc
	ds_add_u32 v10, v32 offset:32768
	v_cndmask_b32_e32 v28, v23, v28, vcc
	v_lshrrev_b32_e32 v10, 20, v31
	v_cmp_eq_u32_e32 vcc, 3, v27
	v_xor_b32_e32 v23, 0xfff, v10
	v_bfe_u32 v27, v43, 6, 2
	v_cndmask_b32_e32 v29, v25, v29, vcc
	v_cndmask_b32_e32 v10, v10, v23, vcc
	s_waitcnt lgkmcnt(5)
	v_pk_add_f32 v[2:3], v[2:3], v[28:29] neg_lo:[0,1] neg_hi:[0,1]
	v_pk_fma_f32 v[28:29], v[20:21], v[96:97], v[16:17] op_sel_hi:[0,1,0]
	v_lshl_add_u32 v10, v10, 2, v11
	v_cndmask_b32_e32 v23, 1, v15, vcc
	v_pk_fma_f32 v[28:29], v[36:37], v[98:99], v[28:29] op_sel_hi:[0,1,1]
	ds_add_u32 v10, v23 offset:32768
	v_exp_f32_e32 v10, v28
	v_exp_f32_e32 v23, v29
	v_pk_fma_f32 v[2:3], v[2:3], v[2:3], v[6:7]
	v_bfe_u32 v25, v43, 4, 2
	v_cmp_eq_u32_e32 vcc, 1, v25
	v_cvt_pknorm_u16_f32 v6, v10, v23
	v_lshrrev_b32_e32 v7, 4, v6
	v_bfe_u32 v28, v6, 4, 12
	v_bitop3_b32 v7, v7, s3, v7 bitop3:0xc
	v_cndmask_b32_e32 v7, v28, v7, vcc
	v_lshl_add_u32 v7, v7, 2, v11
	v_cndmask_b32_e32 v28, 1, v15, vcc
	v_lshrrev_b32_e32 v6, 20, v6
	ds_add_u32 v7, v28
	v_cndmask_b32_e32 v10, 0, v10, vcc
	v_xor_b32_e32 v7, 0xfff, v6
	v_cmp_eq_u32_e32 vcc, 1, v27
	v_cmp_eq_u32_e64 s[8:9], 3, v27
	s_nop 0
	v_cndmask_b32_e32 v6, v6, v7, vcc
	v_lshl_add_u32 v28, v6, 2, v11
	v_pk_fma_f32 v[6:7], v[20:21], v[96:97], v[16:17] op_sel:[1,0,1]
	v_cndmask_b32_e32 v23, 0, v23, vcc
	v_pk_fma_f32 v[6:7], v[36:37], v[98:99], v[6:7] op_sel:[1,0,0]
	s_nop 0
	v_exp_f32_e32 v6, v6
	v_exp_f32_e32 v29, v7
	v_cndmask_b32_e32 v7, 1, v15, vcc
	ds_add_u32 v28, v7
	v_cmp_eq_u32_e32 vcc, 2, v25
	v_cvt_pknorm_u16_f32 v7, v6, v29
	v_lshrrev_b32_e32 v28, 4, v7
	v_bfe_u32 v31, v7, 4, 12
	v_bitop3_b32 v28, v28, s3, v28 bitop3:0xc
	v_cndmask_b32_e32 v10, v10, v6, vcc
	v_lshrrev_b32_e32 v6, 20, v7
	v_cndmask_b32_e32 v28, v31, v28, vcc
	v_cndmask_b32_e32 v31, 1, v15, vcc
	v_xor_b32_e32 v7, 0xfff, v6
	v_cmp_eq_u32_e32 vcc, 2, v27
	v_lshl_add_u32 v28, v28, 2, v11
	ds_add_u32 v28, v31 offset:16384
	v_cndmask_b32_e32 v6, v6, v7, vcc
	v_lshl_add_u32 v28, v6, 2, v11
	v_pk_fma_f32 v[6:7], v[8:9], v[96:97], v[12:13] op_sel_hi:[0,1,0]
	v_pk_fma_f32 v[6:7], v[24:25], v[98:99], v[6:7] op_sel_hi:[0,1,1]
	v_exp_f32_e32 v6, v6
	v_exp_f32_e32 v7, v7
	v_cndmask_b32_e32 v31, 1, v15, vcc
	ds_add_u32 v28, v31 offset:16384
	v_cndmask_b32_e32 v23, v23, v29, vcc
	v_cvt_pknorm_u16_f32 v28, v6, v7
	v_lshrrev_b32_e32 v29, 4, v28
	v_bfe_u32 v31, v28, 4, 12
	v_bitop3_b32 v29, v29, s3, v29 bitop3:0xc
	v_cmp_eq_u32_e32 vcc, 3, v25
	v_cndmask_b32_e64 v27, 1, v15, s[8:9]
	v_cndmask_b32_e64 v7, v23, v7, s[8:9]
	v_cndmask_b32_e32 v25, v31, v29, vcc
	v_lshl_add_u32 v25, v25, 2, v11
	v_cndmask_b32_e32 v29, 1, v15, vcc
	ds_add_u32 v25, v29 offset:32768
	v_lshrrev_b32_e32 v25, 20, v28
	v_xor_b32_e32 v28, 0xfff, v25
	v_cndmask_b32_e64 v25, v25, v28, s[8:9]
	v_lshl_add_u32 v25, v25, 2, v11
	ds_add_u32 v25, v27 offset:32768
	v_cndmask_b32_e32 v6, v10, v6, vcc
	v_pk_add_f32 v[4:5], v[4:5], v[6:7] neg_lo:[0,1] neg_hi:[0,1]
	s_nop 0
	v_pk_fma_f32 v[6:7], v[4:5], v[4:5], v[2:3]
	v_pk_fma_f32 v[2:3], v[100:101], v[20:21], v[16:17] op_sel_hi:[1,0,0]
	v_and_b32_e32 v14, 3, v14
	v_pk_fma_f32 v[2:3], v[102:103], v[36:37], v[2:3] op_sel_hi:[1,0,1]
	v_cmp_eq_u32_e32 vcc, 1, v14
	v_exp_f32_e32 v10, v2
	v_exp_f32_e32 v23, v3
	v_bfe_u32 v25, v42, 2, 2
	ds_read_b128 v[2:5], v1 offset:36864
	v_cvt_pknorm_u16_f32 v27, v10, v23
	v_lshrrev_b32_e32 v28, 4, v27
	v_bfe_u32 v29, v27, 4, 12
	v_bitop3_b32 v28, v28, s3, v28 bitop3:0xc
	v_cndmask_b32_e32 v28, v29, v28, vcc
	v_lshl_add_u32 v28, v28, 2, v11
	v_cndmask_b32_e32 v29, 1, v15, vcc
	v_lshrrev_b32_e32 v27, 20, v27
	ds_add_u32 v28, v29
	v_cndmask_b32_e32 v10, 0, v10, vcc
	v_xor_b32_e32 v28, 0xfff, v27
	v_cmp_eq_u32_e32 vcc, 1, v25
	s_nop 1
	v_cndmask_b32_e32 v27, v27, v28, vcc
	v_pk_fma_f32 v[28:29], v[100:101], v[20:21], v[16:17] op_sel:[0,1,1]
	v_lshl_add_u32 v27, v27, 2, v11
	v_pk_fma_f32 v[28:29], v[102:103], v[36:37], v[28:29] op_sel:[0,1,0]
	v_cndmask_b32_e32 v23, 0, v23, vcc
	v_exp_f32_e32 v28, v28
	v_exp_f32_e32 v31, v29
	v_cndmask_b32_e32 v29, 1, v15, vcc
	ds_add_u32 v27, v29
	v_cmp_eq_u32_e32 vcc, 2, v14
	v_cvt_pknorm_u16_f32 v27, v28, v31
	v_lshrrev_b32_e32 v29, 4, v27
	v_bfe_u32 v32, v27, 4, 12
	v_bitop3_b32 v29, v29, s3, v29 bitop3:0xc
	v_cndmask_b32_e32 v29, v32, v29, vcc
	v_lshrrev_b32_e32 v27, 20, v27
	v_lshl_add_u32 v29, v29, 2, v11
	v_cndmask_b32_e32 v32, 1, v15, vcc
	v_cndmask_b32_e32 v10, v10, v28, vcc
	v_xor_b32_e32 v28, 0xfff, v27
	v_cmp_eq_u32_e32 vcc, 2, v25
	ds_add_u32 v29, v32 offset:16384
	s_nop 0
	v_cndmask_b32_e32 v27, v27, v28, vcc
	v_pk_fma_f32 v[28:29], v[100:101], v[8:9], v[12:13] op_sel_hi:[1,0,0]
	v_lshl_add_u32 v27, v27, 2, v11
	v_pk_fma_f32 v[28:29], v[102:103], v[24:25], v[28:29] op_sel_hi:[1,0,1]
	v_cndmask_b32_e32 v32, 1, v15, vcc
	v_exp_f32_e32 v28, v28
	v_exp_f32_e32 v29, v29
	ds_add_u32 v27, v32 offset:16384
	v_cndmask_b32_e32 v23, v23, v31, vcc
	v_cmp_eq_u32_e32 vcc, 3, v14
	v_cvt_pknorm_u16_f32 v27, v28, v29
	v_lshrrev_b32_e32 v31, 4, v27
	v_bfe_u32 v32, v27, 4, 12
	v_bitop3_b32 v31, v31, s3, v31 bitop3:0xc
	v_cndmask_b32_e32 v14, v32, v31, vcc
	v_lshl_add_u32 v14, v14, 2, v11
	v_cndmask_b32_e32 v31, 1, v15, vcc
	v_cndmask_b32_e32 v28, v10, v28, vcc
	v_lshrrev_b32_e32 v10, 20, v27
	v_cmp_eq_u32_e32 vcc, 3, v25
	ds_add_u32 v14, v31 offset:32768
	v_xor_b32_e32 v14, 0xfff, v10
	v_cndmask_b32_e32 v29, v23, v29, vcc
	v_cndmask_b32_e32 v10, v10, v14, vcc
	s_waitcnt lgkmcnt(5)
	v_pk_add_f32 v[2:3], v[2:3], v[28:29] neg_lo:[0,1] neg_hi:[0,1]
	v_pk_fma_f32 v[28:29], v[20:21], v[104:105], v[16:17] op_sel_hi:[0,1,0]
	v_lshl_add_u32 v10, v10, 2, v11
	v_cndmask_b32_e32 v14, 1, v15, vcc
	v_pk_fma_f32 v[28:29], v[36:37], v[106:107], v[28:29] op_sel_hi:[0,1,1]
	ds_add_u32 v10, v14 offset:32768
	v_exp_f32_e32 v10, v28
	v_exp_f32_e32 v14, v29
	v_pk_fma_f32 v[2:3], v[2:3], v[2:3], v[6:7]
	v_bfe_u32 v23, v42, 4, 2
	v_cmp_eq_u32_e32 vcc, 1, v23
	v_cvt_pknorm_u16_f32 v6, v10, v14
	v_lshrrev_b32_e32 v7, 4, v6
	v_bfe_u32 v27, v6, 4, 12
	v_bitop3_b32 v7, v7, s3, v7 bitop3:0xc
	v_cndmask_b32_e32 v7, v27, v7, vcc
	v_bfe_u32 v25, v42, 6, 2
	v_lshl_add_u32 v7, v7, 2, v11
	v_cndmask_b32_e32 v27, 1, v15, vcc
	v_lshrrev_b32_e32 v6, 20, v6
	ds_add_u32 v7, v27
	v_cndmask_b32_e32 v10, 0, v10, vcc
	v_xor_b32_e32 v7, 0xfff, v6
	v_cmp_eq_u32_e32 vcc, 1, v25
	v_cmp_eq_u32_e64 s[8:9], 3, v25
	s_nop 0
	v_cndmask_b32_e32 v6, v6, v7, vcc
	v_lshl_add_u32 v27, v6, 2, v11
	v_pk_fma_f32 v[6:7], v[20:21], v[104:105], v[16:17] op_sel:[1,0,1]
	v_cndmask_b32_e32 v14, 0, v14, vcc
	v_pk_fma_f32 v[6:7], v[36:37], v[106:107], v[6:7] op_sel:[1,0,0]
	s_nop 0
	v_exp_f32_e32 v6, v6
	v_exp_f32_e32 v28, v7
	v_cndmask_b32_e32 v7, 1, v15, vcc
	ds_add_u32 v27, v7
	v_cmp_eq_u32_e32 vcc, 2, v23
	v_cvt_pknorm_u16_f32 v7, v6, v28
	v_lshrrev_b32_e32 v27, 4, v7
	v_bfe_u32 v29, v7, 4, 12
	v_bitop3_b32 v27, v27, s3, v27 bitop3:0xc
	v_cndmask_b32_e32 v10, v10, v6, vcc
	v_lshrrev_b32_e32 v6, 20, v7
	v_cndmask_b32_e32 v27, v29, v27, vcc
	v_cndmask_b32_e32 v29, 1, v15, vcc
	v_xor_b32_e32 v7, 0xfff, v6
	v_cmp_eq_u32_e32 vcc, 2, v25
	v_lshl_add_u32 v27, v27, 2, v11
	ds_add_u32 v27, v29 offset:16384
	v_cndmask_b32_e32 v6, v6, v7, vcc
	v_lshl_add_u32 v27, v6, 2, v11
	v_pk_fma_f32 v[6:7], v[8:9], v[104:105], v[12:13] op_sel_hi:[0,1,0]
	v_pk_fma_f32 v[6:7], v[24:25], v[106:107], v[6:7] op_sel_hi:[0,1,1]
	v_exp_f32_e32 v6, v6
	v_exp_f32_e32 v7, v7
	v_cndmask_b32_e32 v29, 1, v15, vcc
	ds_add_u32 v27, v29 offset:16384
	v_cndmask_b32_e32 v14, v14, v28, vcc
	v_cvt_pknorm_u16_f32 v27, v6, v7
	v_lshrrev_b32_e32 v28, 4, v27
	v_bfe_u32 v29, v27, 4, 12
	v_bitop3_b32 v28, v28, s3, v28 bitop3:0xc
	v_cmp_eq_u32_e32 vcc, 3, v23
	v_cndmask_b32_e64 v25, 1, v15, s[8:9]
	v_cndmask_b32_e64 v7, v14, v7, s[8:9]
	v_cndmask_b32_e32 v23, v29, v28, vcc
	v_lshl_add_u32 v23, v23, 2, v11
	v_cndmask_b32_e32 v28, 1, v15, vcc
	ds_add_u32 v23, v28 offset:32768
	v_lshrrev_b32_e32 v23, 20, v27
	v_xor_b32_e32 v27, 0xfff, v23
	v_cndmask_b32_e64 v23, v23, v27, s[8:9]
	v_lshl_add_u32 v23, v23, 2, v11
	ds_add_u32 v23, v25 offset:32768
	v_cndmask_b32_e32 v6, v10, v6, vcc
	v_pk_add_f32 v[4:5], v[4:5], v[6:7] neg_lo:[0,1] neg_hi:[0,1]
	s_nop 0
	v_pk_fma_f32 v[6:7], v[4:5], v[4:5], v[2:3]
	v_pk_fma_f32 v[2:3], v[108:109], v[20:21], v[16:17] op_sel_hi:[1,0,0]
	v_and_b32_e32 v18, 3, v18
	v_pk_fma_f32 v[2:3], v[110:111], v[36:37], v[2:3] op_sel_hi:[1,0,1]
	v_cmp_eq_u32_e32 vcc, 1, v18
	v_exp_f32_e32 v10, v2
	v_exp_f32_e32 v14, v3
	ds_read_b128 v[2:5], v1 offset:49152
	v_bfe_u32 v23, v41, 2, 2
	v_cvt_pknorm_u16_f32 v25, v10, v14
	v_lshrrev_b32_e32 v27, 4, v25
	v_bfe_u32 v28, v25, 4, 12
	v_bitop3_b32 v27, v27, s3, v27 bitop3:0xc
	v_cndmask_b32_e32 v27, v28, v27, vcc
	v_lshl_add_u32 v27, v27, 2, v11
	v_cndmask_b32_e32 v28, 1, v15, vcc
	ds_add_u32 v27, v28
	v_lshrrev_b32_e32 v25, 20, v25
	v_pk_fma_f32 v[28:29], v[108:109], v[20:21], v[16:17] op_sel:[0,1,1]
	v_cndmask_b32_e32 v10, 0, v10, vcc
	v_xor_b32_e32 v27, 0xfff, v25
	v_cmp_eq_u32_e32 vcc, 1, v23
	v_pk_fma_f32 v[28:29], v[110:111], v[36:37], v[28:29] op_sel:[0,1,0]
	s_nop 0
	v_cndmask_b32_e32 v25, v25, v27, vcc
	v_exp_f32_e32 v27, v28
	v_exp_f32_e32 v31, v29
	v_lshl_add_u32 v25, v25, 2, v11
	v_cndmask_b32_e32 v28, 1, v15, vcc
	ds_add_u32 v25, v28
	v_cvt_pknorm_u16_f32 v25, v27, v31
	v_lshrrev_b32_e32 v28, 4, v25
	v_cndmask_b32_e32 v14, 0, v14, vcc
	v_bfe_u32 v29, v25, 4, 12
	v_bitop3_b32 v28, v28, s3, v28 bitop3:0xc
	v_cmp_eq_u32_e32 vcc, 2, v18
	v_lshrrev_b32_e32 v25, 20, v25
	s_nop 0
	v_cndmask_b32_e32 v28, v29, v28, vcc
	v_cndmask_b32_e32 v29, 1, v15, vcc
	v_cndmask_b32_e32 v10, v10, v27, vcc
	v_xor_b32_e32 v27, 0xfff, v25
	v_cmp_eq_u32_e32 vcc, 2, v23
	v_lshl_add_u32 v28, v28, 2, v11
	ds_add_u32 v28, v29 offset:16384
	v_cndmask_b32_e32 v25, v25, v27, vcc
	v_lshl_add_u32 v25, v25, 2, v11
	v_pk_fma_f32 v[28:29], v[108:109], v[8:9], v[12:13] op_sel_hi:[1,0,0]
	v_cndmask_b32_e32 v14, v14, v31, vcc
	v_pk_fma_f32 v[28:29], v[110:111], v[24:25], v[28:29] op_sel_hi:[1,0,1]
	s_nop 0
	v_exp_f32_e32 v27, v28
	v_exp_f32_e32 v29, v29
	v_cndmask_b32_e32 v28, 1, v15, vcc
	ds_add_u32 v25, v28 offset:16384
	v_cmp_eq_u32_e32 vcc, 3, v18
	v_cvt_pknorm_u16_f32 v25, v27, v29
	v_lshrrev_b32_e32 v28, 4, v25
	v_bfe_u32 v31, v25, 4, 12
	v_bitop3_b32 v28, v28, s3, v28 bitop3:0xc
	v_cndmask_b32_e32 v18, v31, v28, vcc
	v_lshl_add_u32 v18, v18, 2, v11
	v_cndmask_b32_e32 v28, 1, v15, vcc
	ds_add_u32 v18, v28 offset:32768
	v_cndmask_b32_e32 v28, v10, v27, vcc
	v_lshrrev_b32_e32 v10, 20, v25
	v_cmp_eq_u32_e32 vcc, 3, v23
	v_xor_b32_e32 v18, 0xfff, v10
	v_bfe_u32 v23, v41, 6, 2
	v_cndmask_b32_e32 v29, v14, v29, vcc
	v_cndmask_b32_e32 v10, v10, v18, vcc
	s_waitcnt lgkmcnt(5)
	v_pk_add_f32 v[2:3], v[2:3], v[28:29] neg_lo:[0,1] neg_hi:[0,1]
	v_pk_fma_f32 v[28:29], v[20:21], v[112:113], v[16:17] op_sel_hi:[0,1,0]
	v_lshl_add_u32 v10, v10, 2, v11
	v_cndmask_b32_e32 v18, 1, v15, vcc
	v_pk_fma_f32 v[28:29], v[36:37], v[114:115], v[28:29] op_sel_hi:[0,1,1]
	ds_add_u32 v10, v18 offset:32768
	v_exp_f32_e32 v10, v28
	v_exp_f32_e32 v14, v29
	v_pk_fma_f32 v[2:3], v[2:3], v[2:3], v[6:7]
	v_bfe_u32 v18, v41, 4, 2
	v_cmp_eq_u32_e32 vcc, 1, v18
	v_cvt_pknorm_u16_f32 v6, v10, v14
	v_lshrrev_b32_e32 v7, 4, v6
	v_bfe_u32 v25, v6, 4, 12
	v_bitop3_b32 v7, v7, s3, v7 bitop3:0xc
	v_cndmask_b32_e32 v7, v25, v7, vcc
	v_lshl_add_u32 v7, v7, 2, v11
	v_cndmask_b32_e32 v25, 1, v15, vcc
	v_lshrrev_b32_e32 v6, 20, v6
	ds_add_u32 v7, v25
	v_cndmask_b32_e32 v10, 0, v10, vcc
	v_xor_b32_e32 v7, 0xfff, v6
	v_cmp_eq_u32_e32 vcc, 1, v23
	v_cmp_eq_u32_e64 s[8:9], 3, v23
	s_nop 0
	v_cndmask_b32_e32 v6, v6, v7, vcc
	v_lshl_add_u32 v25, v6, 2, v11
	v_pk_fma_f32 v[6:7], v[20:21], v[112:113], v[16:17] op_sel:[1,0,1]
	v_cndmask_b32_e32 v14, 0, v14, vcc
	v_pk_fma_f32 v[6:7], v[36:37], v[114:115], v[6:7] op_sel:[1,0,0]
	s_nop 0
	v_exp_f32_e32 v6, v6
	v_exp_f32_e32 v27, v7
	v_cndmask_b32_e32 v7, 1, v15, vcc
	ds_add_u32 v25, v7
	v_cmp_eq_u32_e32 vcc, 2, v18
	v_cvt_pknorm_u16_f32 v7, v6, v27
	v_lshrrev_b32_e32 v25, 4, v7
	v_bfe_u32 v28, v7, 4, 12
	v_bitop3_b32 v25, v25, s3, v25 bitop3:0xc
	v_cndmask_b32_e32 v10, v10, v6, vcc
	v_lshrrev_b32_e32 v6, 20, v7
	v_cndmask_b32_e32 v25, v28, v25, vcc
	v_cndmask_b32_e32 v28, 1, v15, vcc
	v_xor_b32_e32 v7, 0xfff, v6
	v_cmp_eq_u32_e32 vcc, 2, v23
	v_lshl_add_u32 v25, v25, 2, v11
	ds_add_u32 v25, v28 offset:16384
	v_cndmask_b32_e32 v6, v6, v7, vcc
	v_lshl_add_u32 v25, v6, 2, v11
	v_pk_fma_f32 v[6:7], v[8:9], v[112:113], v[12:13] op_sel_hi:[0,1,0]
	v_pk_fma_f32 v[6:7], v[24:25], v[114:115], v[6:7] op_sel_hi:[0,1,1]
	v_exp_f32_e32 v6, v6
	v_exp_f32_e32 v7, v7
	v_cndmask_b32_e32 v28, 1, v15, vcc
	ds_add_u32 v25, v28 offset:16384
	v_cndmask_b32_e32 v14, v14, v27, vcc
	v_cvt_pknorm_u16_f32 v25, v6, v7
	v_lshrrev_b32_e32 v27, 4, v25
	v_bfe_u32 v28, v25, 4, 12
	v_bitop3_b32 v27, v27, s3, v27 bitop3:0xc
	v_cmp_eq_u32_e32 vcc, 3, v18
	v_cndmask_b32_e64 v23, 1, v15, s[8:9]
	v_cndmask_b32_e64 v7, v14, v7, s[8:9]
	v_cndmask_b32_e32 v18, v28, v27, vcc
	v_lshl_add_u32 v18, v18, 2, v11
	v_cndmask_b32_e32 v27, 1, v15, vcc
	ds_add_u32 v18, v27 offset:32768
	v_lshrrev_b32_e32 v18, 20, v25
	v_xor_b32_e32 v25, 0xfff, v18
	v_cndmask_b32_e64 v18, v18, v25, s[8:9]
	v_lshl_add_u32 v18, v18, 2, v11
	ds_add_u32 v18, v23 offset:32768
	v_cndmask_b32_e32 v6, v10, v6, vcc
	v_pk_add_f32 v[4:5], v[4:5], v[6:7] neg_lo:[0,1] neg_hi:[0,1]
	s_nop 0
	v_pk_fma_f32 v[6:7], v[4:5], v[4:5], v[2:3]
	v_pk_fma_f32 v[2:3], v[116:117], v[20:21], v[16:17] op_sel_hi:[1,0,0]
	v_and_b32_e32 v18, 3, v22
	v_pk_fma_f32 v[2:3], v[118:119], v[36:37], v[2:3] op_sel_hi:[1,0,1]
	v_cmp_eq_u32_e32 vcc, 1, v18
	v_exp_f32_e32 v10, v2
	v_exp_f32_e32 v14, v3
	v_bfe_u32 v25, v19, 2, 2
	ds_read_b128 v[2:5], v1 offset:61440
	v_cvt_pknorm_u16_f32 v22, v10, v14
	v_lshrrev_b32_e32 v23, 4, v22
	v_bfe_u32 v27, v22, 4, 12
	v_bitop3_b32 v23, v23, s3, v23 bitop3:0xc
	v_cndmask_b32_e32 v23, v27, v23, vcc
	v_lshl_add_u32 v23, v23, 2, v11
	v_cndmask_b32_e32 v27, 1, v15, vcc
	v_lshrrev_b32_e32 v22, 20, v22
	ds_add_u32 v23, v27
	v_cndmask_b32_e32 v10, 0, v10, vcc
	v_xor_b32_e32 v23, 0xfff, v22
	v_cmp_eq_u32_e32 vcc, 1, v25
	s_nop 1
	v_cndmask_b32_e32 v22, v22, v23, vcc
	v_lshl_add_u32 v27, v22, 2, v11
	v_pk_fma_f32 v[22:23], v[116:117], v[20:21], v[16:17] op_sel:[0,1,1]
	v_cndmask_b32_e32 v14, 0, v14, vcc
	v_pk_fma_f32 v[22:23], v[118:119], v[36:37], v[22:23] op_sel:[0,1,0]
	s_nop 0
	v_exp_f32_e32 v22, v22
	v_exp_f32_e32 v28, v23
	v_cndmask_b32_e32 v23, 1, v15, vcc
	ds_add_u32 v27, v23
	v_cmp_eq_u32_e32 vcc, 2, v18
	v_cvt_pknorm_u16_f32 v23, v22, v28
	v_lshrrev_b32_e32 v27, 4, v23
	v_bfe_u32 v29, v23, 4, 12
	v_bitop3_b32 v27, v27, s3, v27 bitop3:0xc
	v_cndmask_b32_e32 v10, v10, v22, vcc
	v_lshrrev_b32_e32 v22, 20, v23
	v_cndmask_b32_e32 v27, v29, v27, vcc
	v_cndmask_b32_e32 v29, 1, v15, vcc
	v_xor_b32_e32 v23, 0xfff, v22
	v_cmp_eq_u32_e32 vcc, 2, v25
	v_lshl_add_u32 v27, v27, 2, v11
	ds_add_u32 v27, v29 offset:16384
	v_cndmask_b32_e32 v22, v22, v23, vcc
	v_lshl_add_u32 v27, v22, 2, v11
	v_pk_fma_f32 v[22:23], v[116:117], v[8:9], v[12:13] op_sel_hi:[1,0,0]
	v_cndmask_b32_e32 v29, 1, v15, vcc
	v_pk_fma_f32 v[22:23], v[118:119], v[24:25], v[22:23] op_sel_hi:[1,0,1]
	ds_add_u32 v27, v29 offset:16384
	v_exp_f32_e32 v22, v22
	v_exp_f32_e32 v23, v23
	v_cndmask_b32_e32 v14, v14, v28, vcc
	v_cmp_eq_u32_e32 vcc, 3, v18
	v_cvt_pknorm_u16_f32 v27, v22, v23
	v_lshrrev_b32_e32 v28, 4, v27
	v_bfe_u32 v29, v27, 4, 12
	v_bitop3_b32 v28, v28, s3, v28 bitop3:0xc
	v_cndmask_b32_e32 v18, v29, v28, vcc
	v_lshl_add_u32 v18, v18, 2, v11
	v_cndmask_b32_e32 v28, 1, v15, vcc
	v_cndmask_b32_e32 v22, v10, v22, vcc
	v_lshrrev_b32_e32 v10, 20, v27
	v_cmp_eq_u32_e32 vcc, 3, v25
	ds_add_u32 v18, v28 offset:32768
	v_xor_b32_e32 v18, 0xfff, v10
	v_cndmask_b32_e32 v23, v14, v23, vcc
	v_cndmask_b32_e32 v10, v10, v18, vcc
	s_waitcnt lgkmcnt(5)
	v_pk_add_f32 v[2:3], v[2:3], v[22:23] neg_lo:[0,1] neg_hi:[0,1]
	v_pk_fma_f32 v[22:23], v[20:21], v[120:121], v[16:17] op_sel_hi:[0,1,0]
	v_lshl_add_u32 v10, v10, 2, v11
	v_cndmask_b32_e32 v18, 1, v15, vcc
	v_pk_fma_f32 v[22:23], v[36:37], v[122:123], v[22:23] op_sel_hi:[0,1,1]
	ds_add_u32 v10, v18 offset:32768
	v_exp_f32_e32 v10, v22
	v_exp_f32_e32 v14, v23
	v_pk_fma_f32 v[2:3], v[2:3], v[2:3], v[6:7]
	v_bfe_u32 v18, v19, 4, 2
	v_cmp_eq_u32_e32 vcc, 1, v18
	v_cvt_pknorm_u16_f32 v6, v10, v14
	v_lshrrev_b32_e32 v7, 4, v6
	v_bfe_u32 v22, v6, 4, 12
	v_bitop3_b32 v7, v7, s3, v7 bitop3:0xc
	v_cndmask_b32_e32 v7, v22, v7, vcc
	v_bfe_u32 v19, v19, 6, 2
	v_lshl_add_u32 v7, v7, 2, v11
	v_cndmask_b32_e32 v22, 1, v15, vcc
	v_lshrrev_b32_e32 v6, 20, v6
	ds_add_u32 v7, v22
	v_cndmask_b32_e32 v10, 0, v10, vcc
	v_xor_b32_e32 v7, 0xfff, v6
	v_cmp_eq_u32_e32 vcc, 1, v19
	v_cmp_eq_u32_e64 s[8:9], 3, v19
	s_nop 0
	v_cndmask_b32_e32 v6, v6, v7, vcc
	v_lshl_add_u32 v22, v6, 2, v11
	v_pk_fma_f32 v[6:7], v[20:21], v[120:121], v[16:17] op_sel:[1,0,1]
	v_cndmask_b32_e32 v14, 0, v14, vcc
	v_pk_fma_f32 v[6:7], v[36:37], v[122:123], v[6:7] op_sel:[1,0,0]
	s_nop 0
	v_exp_f32_e32 v6, v6
	v_exp_f32_e32 v23, v7
	v_cndmask_b32_e32 v7, 1, v15, vcc
	ds_add_u32 v22, v7
	v_cmp_eq_u32_e32 vcc, 2, v18
	v_cvt_pknorm_u16_f32 v7, v6, v23
	v_lshrrev_b32_e32 v22, 4, v7
	v_bfe_u32 v25, v7, 4, 12
	v_bitop3_b32 v22, v22, s3, v22 bitop3:0xc
	v_cndmask_b32_e32 v10, v10, v6, vcc
	v_lshrrev_b32_e32 v6, 20, v7
	v_cndmask_b32_e32 v22, v25, v22, vcc
	v_cndmask_b32_e32 v25, 1, v15, vcc
	v_xor_b32_e32 v7, 0xfff, v6
	v_cmp_eq_u32_e32 vcc, 2, v19
	v_lshl_add_u32 v22, v22, 2, v11
	ds_add_u32 v22, v25 offset:16384
	v_cndmask_b32_e32 v6, v6, v7, vcc
	v_lshl_add_u32 v22, v6, 2, v11
	v_pk_fma_f32 v[6:7], v[8:9], v[120:121], v[12:13] op_sel_hi:[0,1,0]
	v_pk_fma_f32 v[6:7], v[24:25], v[122:123], v[6:7] op_sel_hi:[0,1,1]
	v_exp_f32_e32 v6, v6
	v_exp_f32_e32 v7, v7
	v_cndmask_b32_e32 v25, 1, v15, vcc
	ds_add_u32 v22, v25 offset:16384
	v_cndmask_b32_e32 v14, v14, v23, vcc
	v_cvt_pknorm_u16_f32 v22, v6, v7
	v_lshrrev_b32_e32 v23, 4, v22
	v_bfe_u32 v25, v22, 4, 12
	v_bitop3_b32 v23, v23, s3, v23 bitop3:0xc
	v_cmp_eq_u32_e32 vcc, 3, v18
	v_cndmask_b32_e64 v19, 1, v15, s[8:9]
	v_cndmask_b32_e64 v7, v14, v7, s[8:9]
	v_cndmask_b32_e32 v18, v25, v23, vcc
	v_lshl_add_u32 v18, v18, 2, v11
	v_cndmask_b32_e32 v23, 1, v15, vcc
	ds_add_u32 v18, v23 offset:32768
	v_lshrrev_b32_e32 v18, 20, v22
	v_xor_b32_e32 v22, 0xfff, v18
	v_cndmask_b32_e64 v18, v18, v22, s[8:9]
	v_lshl_add_u32 v18, v18, 2, v11
	ds_add_u32 v18, v19 offset:32768
	v_cndmask_b32_e32 v6, v10, v6, vcc
	v_pk_add_f32 v[4:5], v[4:5], v[6:7] neg_lo:[0,1] neg_hi:[0,1]
	s_nop 0
	v_pk_fma_f32 v[6:7], v[4:5], v[4:5], v[2:3]
	v_pk_fma_f32 v[2:3], v[58:59], v[20:21], v[16:17] op_sel_hi:[1,0,0]
	v_and_b32_e32 v22, 3, v26
	v_pk_fma_f32 v[2:3], v[124:125], v[36:37], v[2:3] op_sel_hi:[1,0,1]
	v_cmp_eq_u32_e32 vcc, 1, v22
	v_exp_f32_e32 v10, v2
	v_exp_f32_e32 v14, v3
	v_bfe_u32 v23, v13, 2, 2
	ds_read_b128 v[2:5], v135
	v_cvt_pknorm_u16_f32 v18, v10, v14
	v_lshrrev_b32_e32 v19, 4, v18
	v_bfe_u32 v25, v18, 4, 12
	v_bitop3_b32 v19, v19, s3, v19 bitop3:0xc
	v_cndmask_b32_e32 v19, v25, v19, vcc
	v_lshl_add_u32 v19, v19, 2, v11
	v_cndmask_b32_e32 v25, 1, v15, vcc
	v_lshrrev_b32_e32 v18, 20, v18
	ds_add_u32 v19, v25
	v_cndmask_b32_e32 v10, 0, v10, vcc
	v_xor_b32_e32 v19, 0xfff, v18
	v_cmp_eq_u32_e32 vcc, 1, v23
	s_nop 1
	v_cndmask_b32_e32 v18, v18, v19, vcc
	v_lshl_add_u32 v25, v18, 2, v11
	v_pk_fma_f32 v[18:19], v[58:59], v[20:21], v[16:17] op_sel:[0,1,1]
	v_cndmask_b32_e32 v14, 0, v14, vcc
	v_pk_fma_f32 v[18:19], v[124:125], v[36:37], v[18:19] op_sel:[0,1,0]
	s_nop 0
	v_exp_f32_e32 v18, v18
	v_exp_f32_e32 v26, v19
	v_cndmask_b32_e32 v19, 1, v15, vcc
	ds_add_u32 v25, v19
	v_cmp_eq_u32_e32 vcc, 2, v22
	v_cvt_pknorm_u16_f32 v19, v18, v26
	v_lshrrev_b32_e32 v25, 4, v19
	v_bfe_u32 v27, v19, 4, 12
	v_bitop3_b32 v25, v25, s3, v25 bitop3:0xc
	v_cndmask_b32_e32 v10, v10, v18, vcc
	v_lshrrev_b32_e32 v18, 20, v19
	v_cndmask_b32_e32 v25, v27, v25, vcc
	v_cndmask_b32_e32 v27, 1, v15, vcc
	v_xor_b32_e32 v19, 0xfff, v18
	v_cmp_eq_u32_e32 vcc, 2, v23
	v_lshl_add_u32 v25, v25, 2, v11
	ds_add_u32 v25, v27 offset:16384
	v_cndmask_b32_e32 v18, v18, v19, vcc
	v_lshl_add_u32 v25, v18, 2, v11
	v_pk_fma_f32 v[18:19], v[58:59], v[8:9], v[12:13] op_sel_hi:[1,0,0]
	v_cndmask_b32_e32 v27, 1, v15, vcc
	v_pk_fma_f32 v[18:19], v[124:125], v[24:25], v[18:19] op_sel_hi:[1,0,1]
	ds_add_u32 v25, v27 offset:16384
	v_exp_f32_e32 v18, v18
	v_exp_f32_e32 v19, v19
	v_cndmask_b32_e32 v14, v14, v26, vcc
	v_cmp_eq_u32_e32 vcc, 3, v22
	v_cvt_pknorm_u16_f32 v25, v18, v19
	v_lshrrev_b32_e32 v26, 4, v25
	v_bfe_u32 v27, v25, 4, 12
	v_bitop3_b32 v26, v26, s3, v26 bitop3:0xc
	v_cndmask_b32_e32 v22, v27, v26, vcc
	v_lshl_add_u32 v22, v22, 2, v11
	v_cndmask_b32_e32 v26, 1, v15, vcc
	v_cndmask_b32_e32 v18, v10, v18, vcc
	v_lshrrev_b32_e32 v10, 20, v25
	v_cmp_eq_u32_e32 vcc, 3, v23
	ds_add_u32 v22, v26 offset:32768
	v_xor_b32_e32 v22, 0xfff, v10
	v_cndmask_b32_e32 v19, v14, v19, vcc
	v_cndmask_b32_e32 v10, v10, v22, vcc
	s_waitcnt lgkmcnt(5)
	v_pk_add_f32 v[2:3], v[2:3], v[18:19] neg_lo:[0,1] neg_hi:[0,1]
	v_pk_fma_f32 v[18:19], v[20:21], v[60:61], v[16:17] op_sel_hi:[0,1,0]
	v_lshl_add_u32 v10, v10, 2, v11
	v_cndmask_b32_e32 v22, 1, v15, vcc
	v_pk_fma_f32 v[18:19], v[36:37], v[126:127], v[18:19] op_sel_hi:[0,1,1]
	ds_add_u32 v10, v22 offset:32768
	v_exp_f32_e32 v10, v18
	v_exp_f32_e32 v14, v19
	v_pk_fma_f32 v[2:3], v[2:3], v[2:3], v[6:7]
	v_bfe_u32 v18, v13, 4, 2
	v_cmp_eq_u32_e32 vcc, 1, v18
	v_cvt_pknorm_u16_f32 v6, v10, v14
	v_lshrrev_b32_e32 v7, 4, v6
	v_bfe_u32 v19, v6, 4, 12
	v_bitop3_b32 v7, v7, s3, v7 bitop3:0xc
	v_cndmask_b32_e32 v7, v19, v7, vcc
	v_bfe_u32 v13, v13, 6, 2
	v_lshl_add_u32 v7, v7, 2, v11
	v_cndmask_b32_e32 v19, 1, v15, vcc
	v_lshrrev_b32_e32 v6, 20, v6
	ds_add_u32 v7, v19
	v_cndmask_b32_e32 v10, 0, v10, vcc
	v_xor_b32_e32 v7, 0xfff, v6
	v_cmp_eq_u32_e32 vcc, 1, v13
	v_cmp_eq_u32_e64 s[8:9], 3, v13
	s_nop 0
	v_cndmask_b32_e32 v6, v6, v7, vcc
	v_lshl_add_u32 v19, v6, 2, v11
	v_pk_fma_f32 v[6:7], v[20:21], v[60:61], v[16:17] op_sel:[1,0,1]
	v_cndmask_b32_e32 v14, 0, v14, vcc
	v_pk_fma_f32 v[6:7], v[36:37], v[126:127], v[6:7] op_sel:[1,0,0]
	s_nop 0
	v_exp_f32_e32 v6, v6
	v_exp_f32_e32 v22, v7
	v_cndmask_b32_e32 v7, 1, v15, vcc
	ds_add_u32 v19, v7
	v_cmp_eq_u32_e32 vcc, 2, v18
	v_cvt_pknorm_u16_f32 v7, v6, v22
	v_lshrrev_b32_e32 v19, 4, v7
	v_bfe_u32 v23, v7, 4, 12
	v_bitop3_b32 v19, v19, s3, v19 bitop3:0xc
	v_cndmask_b32_e32 v10, v10, v6, vcc
	v_lshrrev_b32_e32 v6, 20, v7
	v_cndmask_b32_e32 v19, v23, v19, vcc
	v_cndmask_b32_e32 v23, 1, v15, vcc
	v_xor_b32_e32 v7, 0xfff, v6
	v_cmp_eq_u32_e32 vcc, 2, v13
	v_lshl_add_u32 v19, v19, 2, v11
	ds_add_u32 v19, v23 offset:16384
	v_cndmask_b32_e32 v6, v6, v7, vcc
	v_lshl_add_u32 v19, v6, 2, v11
	v_pk_fma_f32 v[6:7], v[8:9], v[60:61], v[12:13] op_sel_hi:[0,1,0]
	v_pk_fma_f32 v[6:7], v[24:25], v[126:127], v[6:7] op_sel_hi:[0,1,1]
	v_exp_f32_e32 v6, v6
	v_exp_f32_e32 v7, v7
	v_cndmask_b32_e32 v23, 1, v15, vcc
	ds_add_u32 v19, v23 offset:16384
	v_cndmask_b32_e32 v14, v14, v22, vcc
	v_cvt_pknorm_u16_f32 v19, v6, v7
	v_lshrrev_b32_e32 v22, 4, v19
	v_bfe_u32 v23, v19, 4, 12
	v_bitop3_b32 v22, v22, s3, v22 bitop3:0xc
	v_cmp_eq_u32_e32 vcc, 3, v18
	v_cndmask_b32_e64 v7, v14, v7, s[8:9]
	s_nop 0
	v_cndmask_b32_e32 v18, v23, v22, vcc
	v_lshl_add_u32 v18, v18, 2, v11
	v_cndmask_b32_e32 v22, 1, v15, vcc
	ds_add_u32 v18, v22 offset:32768
	v_lshrrev_b32_e32 v18, 20, v19
	v_xor_b32_e32 v19, 0xfff, v18
	v_cndmask_b32_e64 v13, v18, v19, s[8:9]
	v_lshl_add_u32 v13, v13, 2, v11
	v_cndmask_b32_e64 v18, 1, v15, s[8:9]
	ds_add_u32 v13, v18 offset:32768
	v_cndmask_b32_e32 v6, v10, v6, vcc
	v_pk_add_f32 v[4:5], v[4:5], v[6:7] neg_lo:[0,1] neg_hi:[0,1]
	s_nop 0
	v_pk_fma_f32 v[6:7], v[4:5], v[4:5], v[2:3]
	v_pk_fma_f32 v[2:3], v[62:63], v[20:21], v[16:17] op_sel_hi:[1,0,0]
	v_and_b32_e32 v14, 3, v30
	v_pk_fma_f32 v[2:3], v[66:67], v[36:37], v[2:3] op_sel_hi:[1,0,1]
	v_cmp_eq_u32_e32 vcc, 1, v14
	v_exp_f32_e32 v10, v2
	v_exp_f32_e32 v13, v3
	v_bfe_u32 v22, v9, 2, 2
	ds_read_b128 v[2:5], v70
	v_cvt_pknorm_u16_f32 v18, v10, v13
	v_lshrrev_b32_e32 v19, 4, v18
	v_bfe_u32 v23, v18, 4, 12
	v_bitop3_b32 v19, v19, s3, v19 bitop3:0xc
	v_cndmask_b32_e32 v19, v23, v19, vcc
	v_lshl_add_u32 v19, v19, 2, v11
	v_cndmask_b32_e32 v23, 1, v15, vcc
	v_lshrrev_b32_e32 v18, 20, v18
	ds_add_u32 v19, v23
	v_cndmask_b32_e32 v10, 0, v10, vcc
	v_xor_b32_e32 v19, 0xfff, v18
	v_cmp_eq_u32_e32 vcc, 1, v22
	s_nop 1
	v_cndmask_b32_e32 v18, v18, v19, vcc
	v_lshl_add_u32 v23, v18, 2, v11
	v_pk_fma_f32 v[18:19], v[62:63], v[20:21], v[16:17] op_sel:[0,1,1]
	v_cndmask_b32_e32 v13, 0, v13, vcc
	v_pk_fma_f32 v[18:19], v[66:67], v[36:37], v[18:19] op_sel:[0,1,0]
	s_nop 0
	v_exp_f32_e32 v18, v18
	v_exp_f32_e32 v25, v19
	v_cndmask_b32_e32 v19, 1, v15, vcc
	ds_add_u32 v23, v19
	v_cmp_eq_u32_e32 vcc, 2, v14
	v_cvt_pknorm_u16_f32 v19, v18, v25
	v_lshrrev_b32_e32 v23, 4, v19
	v_bfe_u32 v26, v19, 4, 12
	v_bitop3_b32 v23, v23, s3, v23 bitop3:0xc
	v_cndmask_b32_e32 v10, v10, v18, vcc
	v_lshrrev_b32_e32 v18, 20, v19
	v_cndmask_b32_e32 v23, v26, v23, vcc
	v_cndmask_b32_e32 v26, 1, v15, vcc
	v_xor_b32_e32 v19, 0xfff, v18
	v_cmp_eq_u32_e32 vcc, 2, v22
	v_lshl_add_u32 v23, v23, 2, v11
	ds_add_u32 v23, v26 offset:16384
	v_cndmask_b32_e32 v18, v18, v19, vcc
	v_lshl_add_u32 v23, v18, 2, v11
	v_pk_fma_f32 v[18:19], v[62:63], v[8:9], v[12:13] op_sel_hi:[1,0,0]
	v_cndmask_b32_e32 v26, 1, v15, vcc
	v_pk_fma_f32 v[18:19], v[66:67], v[24:25], v[18:19] op_sel_hi:[1,0,1]
	ds_add_u32 v23, v26 offset:16384
	v_exp_f32_e32 v18, v18
	v_exp_f32_e32 v19, v19
	v_cndmask_b32_e32 v13, v13, v25, vcc
	v_cmp_eq_u32_e32 vcc, 3, v14
	v_cvt_pknorm_u16_f32 v23, v18, v19
	v_lshrrev_b32_e32 v25, 4, v23
	v_bfe_u32 v26, v23, 4, 12
	v_bitop3_b32 v25, v25, s3, v25 bitop3:0xc
	v_cndmask_b32_e32 v14, v26, v25, vcc
	v_lshl_add_u32 v14, v14, 2, v11
	v_cndmask_b32_e32 v25, 1, v15, vcc
	v_cndmask_b32_e32 v18, v10, v18, vcc
	v_lshrrev_b32_e32 v10, 20, v23
	v_cmp_eq_u32_e32 vcc, 3, v22
	ds_add_u32 v14, v25 offset:32768
	v_xor_b32_e32 v14, 0xfff, v10
	v_cndmask_b32_e32 v19, v13, v19, vcc
	v_cndmask_b32_e32 v10, v10, v14, vcc
	s_waitcnt lgkmcnt(5)
	v_pk_add_f32 v[2:3], v[2:3], v[18:19] neg_lo:[0,1] neg_hi:[0,1]
	v_pk_fma_f32 v[18:19], v[20:21], v[64:65], v[16:17] op_sel_hi:[0,1,0]
	v_lshl_add_u32 v10, v10, 2, v11
	v_cndmask_b32_e32 v14, 1, v15, vcc
	v_pk_fma_f32 v[18:19], v[36:37], v[68:69], v[18:19] op_sel_hi:[0,1,1]
	ds_add_u32 v10, v14 offset:32768
	v_exp_f32_e32 v10, v18
	v_exp_f32_e32 v13, v19
	v_pk_fma_f32 v[2:3], v[2:3], v[2:3], v[6:7]
	v_bfe_u32 v14, v9, 4, 2
	v_cmp_eq_u32_e32 vcc, 1, v14
	v_cvt_pknorm_u16_f32 v6, v10, v13
	v_lshrrev_b32_e32 v7, 4, v6
	v_bfe_u32 v18, v6, 4, 12
	v_bitop3_b32 v7, v7, s3, v7 bitop3:0xc
	v_cndmask_b32_e32 v7, v18, v7, vcc
	v_bfe_u32 v9, v9, 6, 2
	v_lshl_add_u32 v7, v7, 2, v11
	v_cndmask_b32_e32 v18, 1, v15, vcc
	v_lshrrev_b32_e32 v6, 20, v6
	ds_add_u32 v7, v18
	v_cndmask_b32_e32 v10, 0, v10, vcc
	v_xor_b32_e32 v7, 0xfff, v6
	v_cmp_eq_u32_e32 vcc, 1, v9
	v_cmp_eq_u32_e64 s[8:9], 3, v9
	s_nop 0
	v_cndmask_b32_e32 v6, v6, v7, vcc
	v_lshl_add_u32 v18, v6, 2, v11
	v_pk_fma_f32 v[6:7], v[20:21], v[64:65], v[16:17] op_sel:[1,0,1]
	v_cndmask_b32_e32 v13, 0, v13, vcc
	v_pk_fma_f32 v[6:7], v[36:37], v[68:69], v[6:7] op_sel:[1,0,0]
	s_nop 0
	v_exp_f32_e32 v6, v6
	v_exp_f32_e32 v19, v7
	v_cndmask_b32_e32 v7, 1, v15, vcc
	ds_add_u32 v18, v7
	v_cmp_eq_u32_e32 vcc, 2, v14
	v_cvt_pknorm_u16_f32 v7, v6, v19
	v_lshrrev_b32_e32 v18, 4, v7
	v_bfe_u32 v22, v7, 4, 12
	v_bitop3_b32 v18, v18, s3, v18 bitop3:0xc
	v_cndmask_b32_e32 v10, v10, v6, vcc
	v_lshrrev_b32_e32 v6, 20, v7
	v_cndmask_b32_e32 v18, v22, v18, vcc
	v_cndmask_b32_e32 v22, 1, v15, vcc
	v_xor_b32_e32 v7, 0xfff, v6
	v_cmp_eq_u32_e32 vcc, 2, v9
	v_lshl_add_u32 v18, v18, 2, v11
	ds_add_u32 v18, v22 offset:16384
	v_cndmask_b32_e32 v6, v6, v7, vcc
	v_lshl_add_u32 v18, v6, 2, v11
	v_pk_fma_f32 v[6:7], v[8:9], v[64:65], v[12:13] op_sel_hi:[0,1,0]
	v_pk_fma_f32 v[6:7], v[24:25], v[68:69], v[6:7] op_sel_hi:[0,1,1]
	v_exp_f32_e32 v6, v6
	v_exp_f32_e32 v7, v7
	v_cndmask_b32_e32 v22, 1, v15, vcc
	ds_add_u32 v18, v22 offset:16384
	v_cndmask_b32_e32 v13, v13, v19, vcc
	v_cvt_pknorm_u16_f32 v18, v6, v7
	v_lshrrev_b32_e32 v19, 4, v18
	v_bfe_u32 v22, v18, 4, 12
	v_bitop3_b32 v19, v19, s3, v19 bitop3:0xc
	v_cmp_eq_u32_e32 vcc, 3, v14
	v_cndmask_b32_e64 v7, v13, v7, s[8:9]
	s_nop 0
	v_cndmask_b32_e32 v14, v22, v19, vcc
	v_lshl_add_u32 v14, v14, 2, v11
	v_cndmask_b32_e32 v19, 1, v15, vcc
	ds_add_u32 v14, v19 offset:32768
	v_lshrrev_b32_e32 v14, 20, v18
	v_xor_b32_e32 v18, 0xfff, v14
	v_cndmask_b32_e64 v9, v14, v18, s[8:9]
	v_lshl_add_u32 v9, v9, 2, v11
	v_cndmask_b32_e64 v14, 1, v15, s[8:9]
	ds_add_u32 v9, v14 offset:32768
	v_cndmask_b32_e32 v6, v10, v6, vcc
	v_pk_add_f32 v[4:5], v[4:5], v[6:7] neg_lo:[0,1] neg_hi:[0,1]
	s_nop 0
	v_pk_fma_f32 v[6:7], v[4:5], v[4:5], v[2:3]
	s_and_saveexec_b64 s[8:9], s[4:5]
	s_cbranch_execz .LBB0_60
	v_mov_b32_e32 v22, v20
	v_mov_b32_e32 v23, v20
	v_mov_b32_e32 v24, v16
	v_mov_b32_e32 v25, v16
	v_mov_b32_e32 v18, v36
	v_mov_b32_e32 v19, v36
	v_pk_fma_f32 v[2:3], v[54:55], v[22:23], v[24:25]
	v_add_u32_e32 v1, 0x18000, v1
	v_pk_fma_f32 v[2:3], v[50:51], v[18:19], v[2:3]
	v_bfe_u32 v30, v40, 2, 2
	v_exp_f32_e32 v10, v2
	v_exp_f32_e32 v14, v3
	ds_read_b128 v[2:5], v1
	v_and_b32_e32 v1, 3, v40
	v_cmp_eq_u32_e32 vcc, 1, v1
	v_cvt_pknorm_u16_f32 v28, v10, v14
	v_lshrrev_b32_e32 v29, 4, v28
	v_bfe_u32 v31, v28, 4, 12
	v_bitop3_b32 v29, v29, s3, v29 bitop3:0xc
	v_cndmask_b32_e32 v29, v31, v29, vcc
	v_lshl_add_u32 v29, v29, 2, v11
	v_cndmask_b32_e32 v31, 1, v15, vcc
	v_lshrrev_b32_e32 v28, 20, v28
	ds_add_u32 v29, v31
	v_cndmask_b32_e32 v10, 0, v10, vcc
	v_xor_b32_e32 v29, 0xfff, v28
	v_cmp_eq_u32_e32 vcc, 1, v30
	v_mov_b32_e32 v20, v21
	v_mov_b32_e32 v16, v17
	v_cndmask_b32_e32 v28, v28, v29, vcc
	v_mov_b32_e32 v36, v37
	v_lshl_add_u32 v31, v28, 2, v11
	v_pk_fma_f32 v[28:29], v[54:55], v[20:21], v[16:17]
	v_cndmask_b32_e32 v14, 0, v14, vcc
	v_pk_fma_f32 v[28:29], v[50:51], v[36:37], v[28:29]
	v_mov_b32_e32 v9, v8
	v_exp_f32_e32 v28, v28
	v_exp_f32_e32 v32, v29
	v_cndmask_b32_e32 v29, 1, v15, vcc
	ds_add_u32 v31, v29
	v_cmp_eq_u32_e32 vcc, 2, v1
	v_cvt_pknorm_u16_f32 v29, v28, v32
	v_lshrrev_b32_e32 v31, 4, v29
	v_bfe_u32 v33, v29, 4, 12
	v_bitop3_b32 v31, v31, s3, v31 bitop3:0xc
	v_cndmask_b32_e32 v10, v10, v28, vcc
	v_lshrrev_b32_e32 v28, 20, v29
	v_cndmask_b32_e32 v31, v33, v31, vcc
	v_cndmask_b32_e32 v33, 1, v15, vcc
	v_xor_b32_e32 v29, 0xfff, v28
	v_cmp_eq_u32_e32 vcc, 2, v30
	v_mov_b32_e32 v13, v12
	v_lshl_add_u32 v31, v31, 2, v11
	v_cndmask_b32_e32 v28, v28, v29, vcc
	v_mov_b32_e32 v26, v38
	v_mov_b32_e32 v27, v38
	ds_add_u32 v31, v33 offset:16384
	v_lshl_add_u32 v31, v28, 2, v11
	v_pk_fma_f32 v[28:29], v[54:55], v[8:9], v[12:13]
	v_cndmask_b32_e32 v33, 1, v15, vcc
	v_pk_fma_f32 v[28:29], v[50:51], v[26:27], v[28:29]
	ds_add_u32 v31, v33 offset:16384
	v_exp_f32_e32 v28, v28
	v_exp_f32_e32 v29, v29
	v_cndmask_b32_e32 v14, v14, v32, vcc
	v_cmp_eq_u32_e32 vcc, 3, v1
	v_pk_fma_f32 v[22:23], v[22:23], v[46:47], v[24:25]
	v_cvt_pknorm_u16_f32 v31, v28, v29
	v_lshrrev_b32_e32 v32, 4, v31
	v_bfe_u32 v33, v31, 4, 12
	v_bitop3_b32 v32, v32, s3, v32 bitop3:0xc
	v_cndmask_b32_e32 v1, v33, v32, vcc
	v_lshl_add_u32 v1, v1, 2, v11
	v_cndmask_b32_e32 v32, 1, v15, vcc
	ds_add_u32 v1, v32 offset:32768
	v_lshrrev_b32_e32 v1, 20, v31
	v_cndmask_b32_e32 v28, v10, v28, vcc
	v_xor_b32_e32 v10, 0xfff, v1
	v_cmp_eq_u32_e32 vcc, 3, v30
	v_pk_fma_f32 v[18:19], v[18:19], v[74:75], v[22:23]
	s_nop 0
	v_cndmask_b32_e32 v1, v1, v10, vcc
	v_lshl_add_u32 v1, v1, 2, v11
	v_cndmask_b32_e32 v10, 1, v15, vcc
	ds_add_u32 v1, v10 offset:32768
	v_exp_f32_e32 v1, v18
	v_exp_f32_e32 v10, v19
	v_cndmask_b32_e32 v29, v14, v29, vcc
	s_waitcnt lgkmcnt(6)
	v_pk_add_f32 v[2:3], v[2:3], v[28:29] neg_lo:[0,1] neg_hi:[0,1]
	v_bfe_u32 v14, v40, 4, 2
	v_pk_fma_f32 v[2:3], v[2:3], v[2:3], v[6:7]
	v_cvt_pknorm_u16_f32 v6, v1, v10
	v_lshrrev_b32_e32 v7, 4, v6
	v_bfe_u32 v19, v6, 4, 12
	v_bitop3_b32 v7, v7, s3, v7 bitop3:0xc
	v_cmp_eq_u32_e32 vcc, 1, v14
	v_bfe_u32 v18, v40, 6, 2
	v_lshrrev_b32_e32 v6, 20, v6
	v_cndmask_b32_e32 v7, v19, v7, vcc
	v_lshl_add_u32 v7, v7, 2, v11
	v_cndmask_b32_e32 v19, 1, v15, vcc
	ds_add_u32 v7, v19
	v_cndmask_b32_e32 v1, 0, v1, vcc
	v_xor_b32_e32 v7, 0xfff, v6
	v_cmp_eq_u32_e32 vcc, 1, v18
	v_cmp_eq_u32_e64 s[4:5], 3, v18
	s_nop 0
	v_cndmask_b32_e32 v6, v6, v7, vcc
	v_lshl_add_u32 v19, v6, 2, v11
	v_pk_fma_f32 v[6:7], v[20:21], v[46:47], v[16:17]
	v_cndmask_b32_e32 v10, 0, v10, vcc
	v_pk_fma_f32 v[6:7], v[36:37], v[74:75], v[6:7]
	s_nop 0
	v_exp_f32_e32 v6, v6
	v_exp_f32_e32 v16, v7
	v_cndmask_b32_e32 v7, 1, v15, vcc
	ds_add_u32 v19, v7
	v_cmp_eq_u32_e32 vcc, 2, v14
	v_cvt_pknorm_u16_f32 v7, v6, v16
	v_lshrrev_b32_e32 v17, 4, v7
	v_bfe_u32 v19, v7, 4, 12
	v_bitop3_b32 v17, v17, s3, v17 bitop3:0xc
	v_cndmask_b32_e32 v1, v1, v6, vcc
	v_lshrrev_b32_e32 v6, 20, v7
	v_cndmask_b32_e32 v17, v19, v17, vcc
	v_cndmask_b32_e32 v19, 1, v15, vcc
	v_xor_b32_e32 v7, 0xfff, v6
	v_cmp_eq_u32_e32 vcc, 2, v18
	v_lshl_add_u32 v17, v17, 2, v11
	ds_add_u32 v17, v19 offset:16384
	v_cndmask_b32_e32 v6, v6, v7, vcc
	v_lshl_add_u32 v17, v6, 2, v11
	v_pk_fma_f32 v[6:7], v[8:9], v[46:47], v[12:13]
	v_cndmask_b32_e32 v8, 1, v15, vcc
	v_pk_fma_f32 v[6:7], v[26:27], v[74:75], v[6:7]
	ds_add_u32 v17, v8 offset:16384
	v_exp_f32_e32 v6, v6
	v_exp_f32_e32 v7, v7
	v_cndmask_b32_e32 v8, v10, v16, vcc
	v_cmp_eq_u32_e32 vcc, 3, v14
	v_cvt_pknorm_u16_f32 v9, v6, v7
	v_lshrrev_b32_e32 v10, 4, v9
	v_bfe_u32 v12, v9, 4, 12
	v_bitop3_b32 v10, v10, s3, v10 bitop3:0xc
	v_cndmask_b32_e32 v10, v12, v10, vcc
	v_lshl_add_u32 v10, v10, 2, v11
	v_cndmask_b32_e32 v12, 1, v15, vcc
	v_lshrrev_b32_e32 v9, 20, v9
	ds_add_u32 v10, v12 offset:32768
	v_xor_b32_e32 v10, 0xfff, v9
	v_cndmask_b32_e64 v9, v9, v10, s[4:5]
	v_lshl_add_u32 v9, v9, 2, v11
	v_cndmask_b32_e64 v10, 1, v15, s[4:5]
	ds_add_u32 v9, v10 offset:32768
	v_cndmask_b32_e32 v6, v1, v6, vcc
	v_cndmask_b32_e64 v7, v8, v7, s[4:5]
	v_pk_add_f32 v[4:5], v[4:5], v[6:7] neg_lo:[0,1] neg_hi:[0,1]
	s_nop 0
	v_pk_fma_f32 v[6:7], v[4:5], v[4:5], v[2:3]
.LBB0_60:
	s_or_b64 exec, exec, s[8:9]
	v_add_f32_e32 v1, v6, v7
	v_lshlrev_b32_e32 v3, 4, v0
	s_mul_i32 s4, s2, 0xc000
	v_add_f32_dpp v1, v1, v1 row_ror:8 row_mask:0xf bank_mask:0xf bound_ctrl:1
	s_mul_hi_u32 s5, s2, 0xc000
	s_add_u32 s4, s10, s4
	v_add_f32_dpp v1, v1, v1 row_ror:4 row_mask:0xf bank_mask:0xf bound_ctrl:1
	s_addc_u32 s5, s11, s5
	v_add_u32_e32 v30, 0x670, v3
	v_add_f32_dpp v1, v1, v1 row_ror:2 row_mask:0xf bank_mask:0xf bound_ctrl:1
	v_mov_b32_e32 v22, s4
	v_mov_b32_e32 v23, s5
	v_add_f32_dpp v1, v1, v1 row_ror:1 row_mask:0xf bank_mask:0xf bound_ctrl:1
	v_mov_b32_e32 v21, 0
	v_mov_b32_e32 v20, v3
	v_lshl_add_u64 v[22:23], v[22:23], 0, v[20:21]
	v_readlane_b32 s16, v1, 0
	v_readlane_b32 s18, v1, 16
	v_readlane_b32 s17, v1, 32
	v_readlane_b32 s19, v1, 48
	s_and_saveexec_b64 s[8:9], s[6:7]
	v_mov_b32_e32 v4, s18
	v_mov_b32_e32 v5, s19
	v_pk_add_f32 v[4:5], s[16:17], v[4:5]
	v_lshlrev_b32_e32 v2, 2, v39
	v_add_f32_e32 v1, v4, v5
	ds_write_b32 v2, v1 offset:1536
	s_or_b64 exec, exec, s[8:9]
	s_waitcnt lgkmcnt(0)
	s_barrier
	ds_read_b128 v[4:7], v30
	ds_read_b128 v[8:11], v30 offset:12288
	ds_read_b128 v[12:15], v30 offset:24576
	ds_read_b128 v[16:19], v30 offset:36864
	s_movk_i32 s8, 0x3000
	s_mov_b32 s9, 0
	v_lshl_add_u64 v[24:25], v[22:23], 0, s[8:9]
	s_movk_i32 s8, 0x6000
	v_lshl_add_u64 v[26:27], v[22:23], 0, s[8:9]
	s_mov_b32 s8, 0x9000
	v_lshl_add_u64 v[28:29], v[22:23], 0, s[8:9]
	s_waitcnt lgkmcnt(3)
	global_store_dwordx4 v[22:23], v[4:7], off nt
	s_waitcnt lgkmcnt(2)
	global_store_dwordx4 v[24:25], v[8:11], off nt
	s_waitcnt lgkmcnt(1)
	global_store_dwordx4 v[26:27], v[12:15], off nt
	s_waitcnt lgkmcnt(0)
	global_store_dwordx4 v[28:29], v[16:19], off nt
	s_andn2_b64 exec, exec, s[0:1]
	s_cbranch_execz .Lkf_end
	v_mov_b32_e32 v1, 0
	ds_read_b128 v[2:5], v1 offset:1536
	ds_read_b128 v[6:9], v1 offset:1552
	ds_read_b128 v[10:13], v1 offset:1568
	s_ashr_i32 s3, s2, 31
	s_lshl_b64 s[4:5], s[2:3], 2
	s_add_u32 s4, s12, s4
	s_addc_u32 s5, s13, s5
	s_waitcnt lgkmcnt(2)
	v_add_f32_e32 v2, 0, v2
	v_add_f32_e32 v2, v2, v3
	v_add_f32_e32 v2, v2, v4
	v_add_f32_e32 v2, v2, v5
	s_waitcnt lgkmcnt(1)
	v_add_f32_e32 v2, v2, v6
	v_add_f32_e32 v2, v2, v7
	v_add_f32_e32 v2, v2, v8
	v_add_f32_e32 v2, v2, v9
	s_waitcnt lgkmcnt(0)
	v_add_f32_e32 v2, v2, v10
	v_add_f32_e32 v2, v2, v11
	v_add_f32_e32 v2, v2, v12
	v_add_f32_e32 v2, v2, v13
	global_store_dword v1, v2, s[4:5]

	.amdhsa_kernel _Z7kf_mainPKfPKiPfPjS3_S4_
		.amdhsa_group_segment_fixed_size 1648
		.amdhsa_private_segment_fixed_size 0
		.amdhsa_kernarg_size 48
		.amdhsa_user_sgpr_count 2
		.amdhsa_user_sgpr_dispatch_ptr 0
		.amdhsa_user_sgpr_queue_ptr 0
		.amdhsa_user_sgpr_kernarg_segment_ptr 1
		.amdhsa_user_sgpr_dispatch_id 0
		.amdhsa_user_sgpr_kernarg_preload_length 0
		.amdhsa_user_sgpr_kernarg_preload_offset 0
		.amdhsa_user_sgpr_private_segment_size 0
		.amdhsa_uses_dynamic_stack 0
		.amdhsa_enable_private_segment 0
		.amdhsa_system_sgpr_workgroup_id_x 1
		.amdhsa_system_sgpr_workgroup_id_y 0
		.amdhsa_system_sgpr_workgroup_id_z 0
		.amdhsa_system_sgpr_workgroup_info 0
		.amdhsa_system_vgpr_workitem_id 0
		.amdhsa_next_free_vgpr 160
		.amdhsa_next_free_sgpr 25
		.amdhsa_accum_offset 160
		.amdhsa_reserve_vcc 1
		.amdhsa_float_round_mode_32 0
		.amdhsa_float_round_mode_16_64 0
		.amdhsa_float_denorm_mode_32 3
		.amdhsa_float_denorm_mode_16_64 3
		.amdhsa_dx10_clamp 1
		.amdhsa_ieee_mode 1
		.amdhsa_fp16_overflow 0
		.amdhsa_tg_split 0
		.amdhsa_exception_fp_ieee_invalid_op 0
		.amdhsa_exception_fp_denorm_src 0
		.amdhsa_exception_fp_ieee_div_zero 0
		.amdhsa_exception_fp_ieee_overflow 0
		.amdhsa_exception_fp_ieee_underflow 0
		.amdhsa_exception_fp_ieee_inexact 0
		.amdhsa_exception_int_div_zero 0
	.end_amdhsa_kernel

.LBB4_29:
	s_or_b64 exec, exec, s[12:13]
	s_waitcnt vmcnt(0)
	v_readfirstlane_b32 s3, v2
	v_readfirstlane_b32 s2, v3
	s_nop 0
	v_mov_b32_e32 v2, s3
	s_mov_b32 s6, 5
	v_mov_b32_e32 v3, s2
	v_mad_u64_u32 v[2:3], s[0:1], s4, v4, v[2:3]
	v_and_b32_e32 v0, 0xff, v2
	v_cmp_eq_u64_e32 vcc, s[6:7], v[0:1]
	s_and_b64 exec, exec, vcc
	s_cbranch_execz .LBB4_31
	v_mov_b32_e32 v0, v3
	v_mad_u64_u32 v[0:1], s[0:1], s5, v4, v[0:1]
	v_mov_b32_e32 v3, v0
	v_lshl_add_u64 v[0:1], v[2:3], 0, s[4:5]
	v_ashrrev_i64 v[0:1], 8, v[0:1]
	v_cvt_f64_i32_e32 v[2:3], v1
	v_ldexp_f64 v[2:3], v[2:3], 32
	v_cvt_f64_u32_e32 v[0:1], v0
	v_add_f64 v[0:1], v[2:3], v[0:1]
	s_movk_i32 s0, 0xffe0
	v_ldexp_f64 v[0:1], v[0:1], s0
	v_cvt_f32_f64_e32 v0, v[0:1]
	v_mov_b32_e32 v1, 0
	global_store_dword v1, v0, s[10:11]

amdhsa.kernels:
  - .agpr_count:     0
    .args:
      - .actual_access:  read_only
        .address_space:  global
        .offset:         0
        .size:           8
        .value_kind:     global_buffer
      - .actual_access:  read_only
        .address_space:  global
        .offset:         8
        .size:           8
        .value_kind:     global_buffer
      - .address_space:  global
        .offset:         16
        .size:           8
        .value_kind:     global_buffer
      - .actual_access:  write_only
        .address_space:  global
        .offset:         24
        .size:           8
        .value_kind:     global_buffer
      - .actual_access:  write_only
        .address_space:  global
        .offset:         32
        .size:           8
        .value_kind:     global_buffer
      - .address_space:  global
        .offset:         40
        .size:           8
        .value_kind:     global_buffer
    .group_segment_fixed_size: 1648
    .kernarg_segment_align: 8
    .kernarg_segment_size: 48
    .language:       OpenCL C
    .language_version:
      - 2
      - 0
    .max_flat_workgroup_size: 768
    .name:           _Z7kf_mainPKfPKiPfPjS3_S4_
    .private_segment_fixed_size: 0
    .sgpr_count:     31
    .sgpr_spill_count: 0
    .symbol:         _Z7kf_mainPKfPKiPfPjS3_S4_.kd
    .uniform_work_group_size: 1
    .uses_dynamic_stack: false
    .vgpr_count:     160
    .vgpr_spill_count: 0
    .wavefront_size: 64
  - .agpr_count:     0
    .args:
      - .actual_access:  read_only
        .address_space:  global
        .offset:         0
        .size:           8
        .value_kind:     global_buffer
      - .actual_access:  read_only
        .address_space:  global
        .offset:         8
        .size:           8
        .value_kind:     global_buffer
      - .actual_access:  write_only
        .address_space:  global
        .offset:         16
        .size:           8
        .value_kind:     global_buffer
    .group_segment_fixed_size: 192
    .kernarg_segment_align: 8
    .kernarg_segment_size: 24
    .language:       OpenCL C
    .language_version:
      - 2
      - 0
    .max_flat_workgroup_size: 256
    .name:           _Z8k1_statsPKfPKiPf
    .private_segment_fixed_size: 0
    .sgpr_count:     48
    .sgpr_spill_count: 0
    .symbol:         _Z8k1_statsPKfPKiPf.kd
    .uniform_work_group_size: 1
    .uses_dynamic_stack: false
    .vgpr_count:     61
    .vgpr_spill_count: 0
    .wavefront_size: 64
  - .agpr_count:     0
    .args:
      - .actual_access:  read_only
        .address_space:  global
        .offset:         0
        .size:           8
        .value_kind:     global_buffer
      - .actual_access:  read_only
        .address_space:  global
        .offset:         8
        .size:           8
        .value_kind:     global_buffer
      - .actual_access:  read_only
        .address_space:  global
        .offset:         16
        .size:           8
        .value_kind:     global_buffer
      - .actual_access:  write_only
        .address_space:  global
        .offset:         24
        .size:           8
        .value_kind:     global_buffer
      - .actual_access:  write_only
        .address_space:  global
        .offset:         32
        .size:           8
        .value_kind:     global_buffer
    .group_segment_fixed_size: 1072
    .kernarg_segment_align: 8
    .kernarg_segment_size: 40
    .language:       OpenCL C
    .language_version:
      - 2
      - 0
    .max_flat_workgroup_size: 768
    .name:           _Z7k3_histPKfPKiS0_PjPf
    .private_segment_fixed_size: 0
    .sgpr_count:     51
    .sgpr_spill_count: 0
    .symbol:         _Z7k3_histPKfPKiS0_PjPf.kd
    .uniform_work_group_size: 1
    .uses_dynamic_stack: false
    .vgpr_count:     64
    .vgpr_spill_count: 0
    .wavefront_size: 64
  - .agpr_count:     0
    .args:
      - .actual_access:  read_only
        .address_space:  global
        .offset:         0
        .size:           8
        .value_kind:     global_buffer
      - .actual_access:  write_only
        .address_space:  global
        .offset:         8
        .size:           8
        .value_kind:     global_buffer
    .group_segment_fixed_size: 2048
    .kernarg_segment_align: 8
    .kernarg_segment_size: 16
    .language:       OpenCL C
    .language_version:
      - 2
      - 0
    .max_flat_workgroup_size: 256
    .name:           _Z9k4_reducePKjP15HIP_vector_typeIjLj2EE
    .private_segment_fixed_size: 0
    .sgpr_count:     14
    .sgpr_spill_count: 0
    .symbol:         _Z9k4_reducePKjP15HIP_vector_typeIjLj2EE.kd
    .uniform_work_group_size: 1
    .uses_dynamic_stack: false
    .vgpr_count:     30
    .vgpr_spill_count: 0
    .wavefront_size: 64
  - .agpr_count:     0
    .args:
      - .actual_access:  read_only
        .address_space:  global
        .offset:         0
        .size:           8
        .value_kind:     global_buffer
      - .actual_access:  read_only
        .address_space:  global
        .offset:         8
        .size:           8
        .value_kind:     global_buffer
      - .actual_access:  read_only
        .address_space:  global
        .offset:         16
        .size:           8
        .value_kind:     global_buffer
      - .address_space:  global
        .offset:         24
        .size:           8
        .value_kind:     global_buffer
      - .actual_access:  write_only
        .address_space:  global
        .offset:         32
        .size:           8
        .value_kind:     global_buffer
      - .offset:         40
        .size:           4
        .value_kind:     hidden_block_count_x
      - .offset:         44
        .size:           4
        .value_kind:     hidden_block_count_y
      - .offset:         48
        .size:           4
        .value_kind:     hidden_block_count_z
      - .offset:         52
        .size:           2
        .value_kind:     hidden_group_size_x
      - .offset:         54
        .size:           2
        .value_kind:     hidden_group_size_y
      - .offset:         56
        .size:           2
        .value_kind:     hidden_group_size_z
      - .offset:         58
        .size:           2
        .value_kind:     hidden_remainder_x
      - .offset:         60
        .size:           2
        .value_kind:     hidden_remainder_y
      - .offset:         62
        .size:           2
        .value_kind:     hidden_remainder_z
      - .offset:         80
        .size:           8
        .value_kind:     hidden_global_offset_x
      - .offset:         88
        .size:           8
        .value_kind:     hidden_global_offset_y
      - .offset:         96
        .size:           8
        .value_kind:     hidden_global_offset_z
      - .offset:         104
        .size:           2
        .value_kind:     hidden_grid_dims
    .group_segment_fixed_size: 12544
    .kernarg_segment_align: 8
    .kernarg_segment_size: 296
    .language:       OpenCL C
    .language_version:
      - 2
      - 0
    .max_flat_workgroup_size: 1024
    .name:           _Z8k5_finalPK15HIP_vector_typeIjLj2EEPKfS4_PyPf
    .private_segment_fixed_size: 0
    .sgpr_count:     20
    .sgpr_spill_count: 0
    .symbol:         _Z8k5_finalPK15HIP_vector_typeIjLj2EEPKfS4_PyPf.kd
    .uniform_work_group_size: 1
    .uses_dynamic_stack: false
    .vgpr_count:     34
    .vgpr_spill_count: 0
    .wavefront_size: 64
